# speedup vs baseline: 1.5124x; 1.3775x over previous
_Z4dt_kPKfS0_S0_PKDF16_PDF16_S3_:
	s_load_dwordx8 s[8:15], s[0:1], 0x0
	s_load_dwordx4 s[16:19], s[0:1], 0x20
	v_lshrrev_b32_e32 v3, 6, v0
	v_and_b32_e32 v1, 15, v0
	v_readfirstlane_b32 s20, v3
	v_bfe_u32 v2, v0, 4, 2
	s_lshl_b32 s21, s2, 6
	s_lshl_b32 s22, s3, 7
	s_lshl_b32 s23, s20, 5
	s_add_u32 s23, s23, s22
	s_lshl_b32 s24, s4, 9
	s_add_u32 s24, s24, s23
	s_lshl_b32 s24, s24, 13
	s_lshl_b32 s25, s21, 1
	s_add_u32 s24, s24, s25
	v_lshrrev_b32_e32 v60, 2, v0
	v_and_b32_e32 v61, 3, v0
	v_lshlrev_b32_e32 v61, 4, v61
	s_lshl_b32 s26, s4, 12
	s_add_u32 s26, s26, s21
	v_add_u32_e32 v62, s26, v60
	v_lshl_add_u32 v62, v62, 6, v61
	v_add_u32_e32 v63, s22, v60
	v_lshl_add_u32 v63, v63, 6, v61
	v_mul_u32_u24_e32 v64, 80, v60
	v_add_u32_e32 v64, v64, v61
	v_and_b32_e32 v65, 63, v0
	v_lshrrev_b32_e32 v66, 3, v65
	v_and_b32_e32 v67, 7, v65
	v_lshlrev_b32_e32 v67, 4, v67
	v_lshl_add_u32 v68, v66, 13, v67
	v_add_u32_e32 v68, s24, v68
	s_mul_i32 s27, s20, 0x3600
	v_mul_u32_u24_e32 v90, 144, v66
	v_add_u32_e32 v90, v90, v67
	v_add_u32_e32 v90, s27, v90
	s_waitcnt lgkmcnt(0)
	global_load_dwordx4 v[4:7], v62, s[8:9]
	global_load_dwordx4 v[8:11], v63, s[10:11]
	v_add_u32_e32 v75, 0x1000, v63
	global_load_dwordx4 v[12:15], v75, s[10:11]
	v_add_u32_e32 v92, 0, v68
	v_add_u32_e32 v93, 65536, v68
	v_add_u32_e32 v94, 131072, v68
	v_add_u32_e32 v95, 196608, v68
	global_load_dwordx4 v[16:19], v92, s[14:15]
	global_load_dwordx4 v[20:23], v93, s[14:15]
	global_load_dwordx4 v[24:27], v94, s[14:15]
	global_load_dwordx4 v[28:31], v95, s[14:15]
	s_lshl_b32 s28, s23, 2
	v_lshlrev_b32_e32 v74, 4, v2
	v_add_u32_e32 v74, s28, v74
	global_load_dwordx4 v[32:35], v74, s[12:13]
	global_load_dwordx4 v[36:39], v74, s[12:13] offset:64
	s_lshl_b32 s29, s20, 5
	v_add_u32_e32 v80, s29, v1
	v_mul_u32_u24_e32 v80, 80, v80
	v_lshl_add_u32 v80, v2, 2, v80
	v_add_u32_e32 v80, 60416, v80
	v_mul_u32_u24_e32 v81, 80, v1
	v_lshl_add_u32 v81, v2, 2, v81
	v_add_u32_e32 v81, 55296, v81
	v_mul_u32_u24_e32 v82, 576, v2
	v_lshl_add_u32 v82, v1, 1, v82
	v_add_u32_e32 v82, s27, v82
	s_mov_b32 s30, 0xbfb8aa3b
	s_mov_b32 s31, 0x3f317217
	s_mov_b32 s33, 0x42800000
	s_waitcnt vmcnt(8)
	ds_write_b128 v64, v[4:7] offset:55296
	s_waitcnt vmcnt(7)
	ds_write_b128 v64, v[8:11] offset:60416
	s_waitcnt vmcnt(6)
	v_add_u32_e32 v76, 0x1400, v64
	ds_write_b128 v76, v[12:15] offset:60416
	s_waitcnt vmcnt(5)
	ds_write_b128 v90, v[16:19] offset:0
	s_waitcnt vmcnt(4)
	ds_write_b128 v90, v[20:23] offset:1152
	s_waitcnt vmcnt(3)
	ds_write_b128 v90, v[24:27] offset:2304
	s_waitcnt vmcnt(2)
	ds_write_b128 v90, v[28:31] offset:3456
	s_waitcnt vmcnt(0) lgkmcnt(0)
	s_barrier
	v_mov_b32_e32 v40, v32
	v_mov_b32_e32 v41, v33
	v_mov_b32_e32 v42, v34
	v_mov_b32_e32 v43, v35
	s_mov_b32 s34, 0
.Ldt_nf:
	ds_read2_b32 v[44:45], v80 offset1:4
	ds_read2_b32 v[46:47], v80 offset0:8 offset1:12
	s_mov_b32 s35, 0
.Ldt_mf:
	ds_read2_b32 v[48:49], v81 offset1:4
	ds_read2_b32 v[50:51], v81 offset0:8 offset1:12
	ds_read_u16 v56, v82
	ds_read_u16 v57, v82 offset:144
	ds_read_u16 v58, v82 offset:288
	ds_read_u16 v59, v82 offset:432
	s_waitcnt lgkmcnt(4)
	v_mfma_f32_16x16x4_f32 v[52:55], v44, v48, 0
	v_mfma_f32_16x16x4_f32 v[52:55], v45, v49, v[52:55]
	v_mfma_f32_16x16x4_f32 v[52:55], v46, v50, v[52:55]
	v_mfma_f32_16x16x4_f32 v[52:55], v47, v51, v[52:55]
	s_waitcnt lgkmcnt(0)
	v_cvt_f32_f16_e32 v56, v56
	v_cvt_f32_f16_e32 v57, v57
	v_cvt_f32_f16_e32 v58, v58
	v_cvt_f32_f16_e32 v59, v59
	s_nop 7
	v_add_f32_e32 v60, v52, v40
	v_add_f32_e32 v61, v53, v41
	v_add_f32_e32 v62, v54, v42
	v_add_f32_e32 v63, v55, v43
	v_mul_f32_e64 v64, |v60|, s30
	v_mul_f32_e64 v65, |v61|, s30
	v_mul_f32_e64 v66, |v62|, s30
	v_mul_f32_e64 v67, |v63|, s30
	v_exp_f32_e32 v64, v64
	v_exp_f32_e32 v65, v65
	v_exp_f32_e32 v66, v66
	v_exp_f32_e32 v67, v67
	v_add_f32_e32 v64, 1.0, v64
	v_add_f32_e32 v65, 1.0, v65
	v_add_f32_e32 v66, 1.0, v66
	v_add_f32_e32 v67, 1.0, v67
	v_log_f32_e32 v64, v64
	v_log_f32_e32 v65, v65
	v_log_f32_e32 v66, v66
	v_log_f32_e32 v67, v67
	v_max_f32_e32 v60, 0, v60
	v_max_f32_e32 v61, 0, v61
	v_max_f32_e32 v62, 0, v62
	v_max_f32_e32 v63, 0, v63
	v_mul_f32_e32 v68, 0x3f317217, v64
	v_mul_f32_e32 v69, 0x3f317217, v65
	v_mul_f32_e32 v70, 0x3f317217, v66
	v_mul_f32_e32 v71, 0x3f317217, v67
	v_fma_f32 v68, v64, s31, -v68
	v_fma_f32 v69, v65, s31, -v69
	v_fma_f32 v70, v66, s31, -v70
	v_fma_f32 v71, v67, s31, -v71
	v_fmac_f32_e32 v68, 0x3377d1cf, v64
	v_fmac_f32_e32 v69, 0x3377d1cf, v65
	v_fmac_f32_e32 v70, 0x3377d1cf, v66
	v_fmac_f32_e32 v71, 0x3377d1cf, v67
	v_fmac_f32_e32 v68, 0x3f317217, v64
	v_fmac_f32_e32 v69, 0x3f317217, v65
	v_fmac_f32_e32 v70, 0x3f317217, v66
	v_fmac_f32_e32 v71, 0x3f317217, v67
	v_add_f32_e32 v60, v60, v68
	v_add_f32_e32 v61, v61, v69
	v_add_f32_e32 v62, v62, v70
	v_add_f32_e32 v63, v63, v71
	v_cvt_f16_f32_e32 v72, v60
	v_cvt_f16_f32_e32 v73, v61
	v_cvt_f16_f32_e32 v74, v62
	v_cvt_f16_f32_e32 v75, v63
	v_mul_f32_e32 v56, v60, v56
	v_mul_f32_e32 v57, v61, v57
	v_mul_f32_e32 v58, v62, v58
	v_mul_f32_e32 v59, v63, v59
	v_fma_mixlo_f16 v56, v56, s33, 0
	v_fma_mixlo_f16 v57, v57, s33, 0
	v_fma_mixlo_f16 v58, v58, s33, 0
	v_fma_mixlo_f16 v59, v59, s33, 0
	ds_write_b16 v82, v72 offset:4608
	ds_write_b16 v82, v56 offset:9216
	ds_write_b16 v82, v73 offset:4752
	ds_write_b16 v82, v57 offset:9360
	ds_write_b16 v82, v74 offset:4896
	ds_write_b16 v82, v58 offset:9504
	ds_write_b16 v82, v75 offset:5040
	ds_write_b16 v82, v59 offset:9648
	v_add_u32_e32 v81, 0x500, v81
	v_add_u32_e32 v82, 32, v82
	s_add_u32 s35, s35, 1
	s_cmp_lt_u32 s35, 4
	s_cbranch_scc1 .Ldt_mf
	v_add_u32_e32 v81, 0xffffec00, v81
	v_add_u32_e32 v82, 0x880, v82
	v_add_u32_e32 v80, 0x500, v80
	v_mov_b32_e32 v40, v36
	v_mov_b32_e32 v41, v37
	v_mov_b32_e32 v42, v38
	v_mov_b32_e32 v43, v39
	s_add_u32 s34, s34, 1
	s_cmp_lt_u32 s34, 2
	s_cbranch_scc1 .Ldt_nf
	s_waitcnt lgkmcnt(0)
	s_barrier
	ds_read_b128 v[4:7], v90 offset:4608
	ds_read_b128 v[8:11], v90 offset:9216
	ds_read_b128 v[12:15], v90 offset:5760
	ds_read_b128 v[16:19], v90 offset:10368
	ds_read_b128 v[20:23], v90 offset:6912
	ds_read_b128 v[24:27], v90 offset:11520
	ds_read_b128 v[28:31], v90 offset:8064
	ds_read_b128 v[32:35], v90 offset:12672
	s_waitcnt lgkmcnt(7)
	global_store_dwordx4 v92, v[4:7], s[16:17]
	s_waitcnt lgkmcnt(6)
	global_store_dwordx4 v92, v[8:11], s[18:19]
	s_waitcnt lgkmcnt(5)
	global_store_dwordx4 v93, v[12:15], s[16:17]
	s_waitcnt lgkmcnt(4)
	global_store_dwordx4 v93, v[16:19], s[18:19]
	s_waitcnt lgkmcnt(3)
	global_store_dwordx4 v94, v[20:23], s[16:17]
	s_waitcnt lgkmcnt(2)
	global_store_dwordx4 v94, v[24:27], s[18:19]
	s_waitcnt lgkmcnt(1)
	global_store_dwordx4 v95, v[28:31], s[16:17]
	s_waitcnt lgkmcnt(0)
	global_store_dwordx4 v95, v[32:35], s[18:19]
	s_endpgm

	.amdhsa_kernel _Z4dt_kPKfS0_S0_PKDF16_PDF16_S3_
		.amdhsa_group_segment_fixed_size 70656
		.amdhsa_private_segment_fixed_size 0
		.amdhsa_kernarg_size 48
		.amdhsa_user_sgpr_count 2
		.amdhsa_user_sgpr_dispatch_ptr 0
		.amdhsa_user_sgpr_queue_ptr 0
		.amdhsa_user_sgpr_kernarg_segment_ptr 1
		.amdhsa_user_sgpr_dispatch_id 0
		.amdhsa_user_sgpr_kernarg_preload_length 0
		.amdhsa_user_sgpr_kernarg_preload_offset 0
		.amdhsa_user_sgpr_private_segment_size 0
		.amdhsa_uses_dynamic_stack 0
		.amdhsa_enable_private_segment 0
		.amdhsa_system_sgpr_workgroup_id_x 1
		.amdhsa_system_sgpr_workgroup_id_y 1
		.amdhsa_system_sgpr_workgroup_id_z 1
		.amdhsa_system_sgpr_workgroup_info 0
		.amdhsa_system_vgpr_workitem_id 0
		.amdhsa_next_free_vgpr 96
		.amdhsa_next_free_sgpr 96
		.amdhsa_accum_offset 96
		.amdhsa_reserve_vcc 1
		.amdhsa_float_round_mode_32 0
		.amdhsa_float_round_mode_16_64 0
		.amdhsa_float_denorm_mode_32 3
		.amdhsa_float_denorm_mode_16_64 3
		.amdhsa_dx10_clamp 1
		.amdhsa_ieee_mode 1
		.amdhsa_fp16_overflow 0
		.amdhsa_tg_split 0
		.amdhsa_exception_fp_ieee_invalid_op 0
		.amdhsa_exception_fp_denorm_src 0
		.amdhsa_exception_fp_ieee_div_zero 0
		.amdhsa_exception_fp_ieee_overflow 0
		.amdhsa_exception_fp_ieee_underflow 0
		.amdhsa_exception_fp_ieee_inexact 0
		.amdhsa_exception_int_div_zero 0
	.end_amdhsa_kernel

_Z6scan_kPKDF16_S0_S0_S0_PKfPf:
	s_load_dwordx8 s[4:11], s[0:1], 0x0
	s_load_dwordx4 s[12:15], s[0:1], 0x20
	v_and_b32_e32 v1, 63, v0
	v_lshrrev_b32_e32 v2, 6, v0
	s_nop 1
	v_readfirstlane_b32 s16, v2
	s_lshr_b32 s17, s2, 7
	s_and_b32 s18, s2, 127
	s_lshl_b32 s18, s18, 2
	s_add_u32 s18, s18, s16
	s_lshl_b32 s19, s17, 9
	s_add_u32 s19, s19, s18
	s_mul_i32 s28, s16, 4608
	s_add_u32 s28, s28, 67584
	s_lshl_b32 s32, s16, 10
	s_add_u32 s33, s32, 0x1000
	s_add_u32 s34, s32, 0x2000
	s_add_u32 s35, s32, 0x3000
	s_mov_b32 s46, 0x200
	s_mov_b32 s47, 0
	s_mov_b32 s40, 0
	v_lshlrev_b32_e32 v2, 4, v1
	v_add_u32_e32 v3, 0x1000, v2
	v_add_u32_e32 v4, 0x2000, v2
	v_add_u32_e32 v5, 0x3000, v2
	v_lshlrev_b32_e32 v6, 2, v1
	v_lshlrev_b32_e32 v7, 1, v1
	v_and_b32_e32 v20, 7, v1
	v_lshlrev_b32_e32 v20, 1, v20
	v_add_u32_e32 v8, v2, v20
	v_add_u32_e32 v8, s28, v8
	v_and_b32_e32 v20, 3, v1
	v_bfe_u32 v21, v1, 3, 2
	v_lshl_add_u32 v20, v21, 2, v20
	v_lshrrev_b32_e32 v21, 5, v1
	v_bfe_u32 v22, v1, 2, 1
	v_bfe_u32 v23, v1, 4, 1
	v_cmp_eq_u32_e64 s[48:49], v21, v22
	v_cmp_eq_u32_e64 s[50:51], 0, v23
	s_nop 1
	s_and_b64 s[52:53], s[48:49], s[50:51]
	s_andn2_b64 s[54:55], s[48:49], s[50:51]
	v_mov_b32_e32 v24, 65536
	v_lshlrev_b32_e32 v25, 1, v20
	v_add_u32_e32 v25, s28, v25
	v_add_u32_e32 v26, 0x100, v25
	s_nop 1
	v_cndmask_b32_e64 v9, v24, v25, s[48:49]
	v_cndmask_b32_e64 v10, v24, v26, s[48:49]
	v_lshlrev_b32_e32 v25, 4, v20
	v_add_u32_e32 v25, s28, v25
	v_add_u32_e32 v25, 0x200, v25
	v_add_u32_e32 v26, 0x800, v25
	v_cndmask_b32_e64 v11, v24, v25, s[48:49]
	v_cndmask_b32_e64 v13, v24, v26, s[48:49]
	v_mov_b32_e32 v15, 1.0
	v_and_b32_e32 v89, 15, v1
	s_mov_b32 s42, 0xffff
	s_mov_b32 s43, 0
	v_xor_b32_e32 v86, 16, v1
	v_lshlrev_b32_e32 v86, 2, v86
	v_xor_b32_e32 v87, 32, v1
	v_lshlrev_b32_e32 v87, 2, v87
	s_waitcnt lgkmcnt(0)
	s_lshl_b32 s30, s19, 13
	s_add_u32 s24, s4, s30
	s_addc_u32 s25, s5, 0
	s_add_u32 s26, s6, s30
	s_addc_u32 s27, s7, 0
	s_lshl_b32 s30, s17, 19
	s_add_u32 s30, s30, s32
	s_add_u32 s20, s8, s30
	s_addc_u32 s21, s9, 0
	s_add_u32 s22, s10, s30
	s_addc_u32 s23, s11, 0
	s_lshl_b32 s30, s18, 8
	s_add_u32 s12, s12, s30
	s_addc_u32 s13, s13, 0
	global_load_dword v90, v6, s[12:13]
	global_load_ushort v18, v7, s[26:27]
	global_load_ushort v19, v7, s[26:27] offset:128
	s_lshl_b32 s30, s19, 14
	s_add_u32 s14, s14, s30
	s_addc_u32 s15, s15, 0
	v_and_b32_e32 v30, 15, v1
	v_lshlrev_b32_e32 v30, 2, v30
	v_mov_b32_e32 v31, 0
	v_lshl_add_u64 v[16:17], s[14:15], 0, v[30:31]
	v_mov_b32_e32 v36, 0
	v_mov_b32_e32 v37, 0
	v_mov_b32_e32 v38, 0
	v_mov_b32_e32 v39, 0
	v_add_u32_e32 v29, 65536, v2
	ds_write_b128 v29, v[36:39]
	ds_write_b128 v29, v[36:39] offset:1024
	v_add_u32_e32 v29, s28, v2
	ds_write_b128 v29, v[36:39] offset:512
	ds_write_b128 v29, v[36:39] offset:1536
	ds_write_b128 v29, v[36:39] offset:2560
	ds_write_b128 v29, v[36:39] offset:3584
	s_mov_b32 m0, s32
	s_nop 0
	global_load_lds_dwordx4 v2, s[20:21]
	s_add_i32 m0, s32, 32768
	s_nop 0
	global_load_lds_dwordx4 v2, s[22:23]
	s_mov_b32 m0, s33
	s_nop 0
	global_load_lds_dwordx4 v3, s[20:21]
	s_add_i32 m0, s33, 32768
	s_nop 0
	global_load_lds_dwordx4 v3, s[22:23]
	s_mov_b32 m0, s34
	s_nop 0
	global_load_lds_dwordx4 v4, s[20:21]
	s_add_i32 m0, s34, 32768
	s_nop 0
	global_load_lds_dwordx4 v4, s[22:23]
	s_mov_b32 m0, s35
	s_nop 0
	global_load_lds_dwordx4 v5, s[20:21]
	s_add_i32 m0, s35, 32768
	s_nop 0
	global_load_lds_dwordx4 v5, s[22:23]
	s_mov_b32 m0, s28
	s_nop 0
	global_load_lds_dword v6, s[24:25]
	s_add_u32 s20, s20, 0x4000
	s_addc_u32 s21, s21, 0
	s_add_u32 s22, s22, 0x4000
	s_addc_u32 s23, s23, 0
	s_add_u32 s24, s24, 0x100
	s_addc_u32 s25, s25, 0
	s_add_i32 m0, s32, 16384
	s_nop 0
	global_load_lds_dwordx4 v2, s[20:21]
	s_add_i32 m0, s32, 49152
	s_nop 0
	global_load_lds_dwordx4 v2, s[22:23]
	s_add_i32 m0, s33, 16384
	s_nop 0
	global_load_lds_dwordx4 v3, s[20:21]
	s_add_i32 m0, s33, 49152
	s_nop 0
	global_load_lds_dwordx4 v3, s[22:23]
	s_add_i32 m0, s34, 16384
	s_nop 0
	global_load_lds_dwordx4 v4, s[20:21]
	s_add_i32 m0, s34, 49152
	s_nop 0
	global_load_lds_dwordx4 v4, s[22:23]
	s_add_i32 m0, s35, 16384
	s_nop 0
	global_load_lds_dwordx4 v5, s[20:21]
	s_add_i32 m0, s35, 49152
	s_nop 0
	global_load_lds_dwordx4 v5, s[22:23]
	s_add_i32 m0, s28, 0x100
	s_nop 0
	global_load_lds_dword v6, s[24:25]
	s_add_u32 s20, s20, 0x4000
	s_addc_u32 s21, s21, 0
	s_add_u32 s22, s22, 0x4000
	s_addc_u32 s23, s23, 0
	s_add_u32 s24, s24, 0x100
	s_addc_u32 s25, s25, 0
	s_mov_b32 s3, 0x3fb8aa3b
	s_waitcnt vmcnt(20)
	v_mul_f32_e32 v91, 0x3fb8aa3b, v90
	v_fma_f32 v92, v90, s3, -v91
	v_rndne_f32_e32 v93, v91
	v_fmamk_f32 v92, v90, 0x32a5705f, v92
	v_sub_f32_e32 v91, v91, v93
	v_add_f32_e32 v91, v91, v92
	v_exp_f32_e32 v91, v91
	v_cvt_i32_f32_e32 v92, v93
	s_mov_b32 s3, 0xc2ce8ed0
	v_cmp_ngt_f32_e32 vcc, s3, v90
	s_mov_b32 s3, 0x42b17218
	v_ldexp_f32 v91, v91, v92
	v_cndmask_b32_e32 v91, 0, v91, vcc
	v_mov_b32_e32 v92, 0x7f800000
	v_cmp_nlt_f32_e32 vcc, s3, v90
	s_mov_b32 s3, 0xbfb8aa3b
	s_nop 1
	v_cndmask_b32_e32 v90, v92, v91, vcc
	v_mov_b32_e32 v93, 0
	s_nop 0
	v_fma_mixlo_f16 v93, v90, s3, 0
	v_and_b32_e32 v28, 0xffff, v93
	v_mov_b32_e32 v29, 0
	v_mov_b32_e32 v30, 0
	v_mov_b32_e32 v31, 0
	v_mov_b32_e32 v32, 0
	v_mov_b32_e32 v33, 0
	v_mov_b32_e32 v34, 0
	v_mov_b32_e32 v35, 0
	v_mov_b32_e32 v96, 0x1c00
	v_mov_b32_e32 v97, 0x1c000000
	v_cmp_eq_u32_e32 vcc, 0, v89
	s_nop 1
	v_cndmask_b32_e32 v20, 0, v96, vcc
	v_cmp_eq_u32_e32 vcc, 1, v89
	s_nop 1
	v_cndmask_b32_e32 v20, v20, v97, vcc
	v_cmp_eq_u32_e32 vcc, 2, v89
	s_nop 1
	v_cndmask_b32_e32 v21, 0, v96, vcc
	v_cmp_eq_u32_e32 vcc, 3, v89
	s_nop 1
	v_cndmask_b32_e32 v21, v21, v97, vcc
	v_cmp_eq_u32_e32 vcc, 4, v89
	s_nop 1
	v_cndmask_b32_e32 v22, 0, v96, vcc
	v_cmp_eq_u32_e32 vcc, 5, v89
	s_nop 1
	v_cndmask_b32_e32 v22, v22, v97, vcc
	v_cmp_eq_u32_e32 vcc, 6, v89
	s_nop 1
	v_cndmask_b32_e32 v23, 0, v96, vcc
	v_cmp_eq_u32_e32 vcc, 7, v89
	s_nop 1
	v_cndmask_b32_e32 v23, v23, v97, vcc
	v_cmp_eq_u32_e32 vcc, 8, v89
	s_nop 1
	v_cndmask_b32_e32 v24, 0, v96, vcc
	v_cmp_eq_u32_e32 vcc, 9, v89
	s_nop 1
	v_cndmask_b32_e32 v24, v24, v97, vcc
	v_cmp_eq_u32_e32 vcc, 10, v89
	s_nop 1
	v_cndmask_b32_e32 v25, 0, v96, vcc
	v_cmp_eq_u32_e32 vcc, 11, v89
	s_nop 1
	v_cndmask_b32_e32 v25, v25, v97, vcc
	v_cmp_eq_u32_e32 vcc, 12, v89
	s_nop 1
	v_cndmask_b32_e32 v26, 0, v96, vcc
	v_cmp_eq_u32_e32 vcc, 13, v89
	s_nop 1
	v_cndmask_b32_e32 v26, v26, v97, vcc
	v_cmp_eq_u32_e32 vcc, 14, v89
	s_nop 1
	v_cndmask_b32_e32 v27, 0, v96, vcc
	v_cmp_eq_u32_e32 vcc, 15, v89
	s_nop 1
	v_cndmask_b32_e32 v27, v27, v97, vcc
	v_mov_b32_e32 v191, 0
	v_mov_b32_e32 v85, 0
	v_mov_b32_e32 v88, 0
	v_mov_b32_e32 v84, 0
	v_mov_b32_e32 v68, 0
	v_mov_b32_e32 v69, 0
	v_mov_b32_e32 v70, 0
	v_mov_b32_e32 v71, 0
	v_mov_b32_e32 v72, 0
	v_mov_b32_e32 v73, 0
	v_mov_b32_e32 v74, 0
	v_mov_b32_e32 v75, 0
	v_mov_b32_e32 v76, 0
	v_mov_b32_e32 v77, 0
	v_mov_b32_e32 v78, 0
	v_mov_b32_e32 v79, 0
	v_mov_b32_e32 v80, 0
	v_mov_b32_e32 v81, 0
	v_mov_b32_e32 v82, 0
	v_mov_b32_e32 v83, 0
	s_waitcnt vmcnt(18)
	v_add_u32_e32 v8, 0x200, v8
	v_add_u32_e32 v94, 0x800, v8
	v_mov_b32_e32 v92, v2
	v_add_u32_e32 v93, 0x4000, v2
	s_mov_b32 s29, s28
	ds_write_b16 v8, v18
	ds_write_b16 v8, v19 offset:1024
	s_add_u32 s26, s26, 0x100
	s_addc_u32 s27, s27, 0
	global_load_ushort v18, v7, s[26:27]
	global_load_ushort v19, v7, s[26:27] offset:128
	s_add_u32 s26, s26, 0x100
	s_addc_u32 s27, s27, 0
	s_waitcnt vmcnt(0)
	s_waitcnt lgkmcnt(0)
	s_barrier
	ds_read_b128 v[52:55], v92 offset:32768
	ds_read_b128 v[56:59], v92 offset:33792
	ds_read_u16 v32, v9 offset:0
	ds_read_b128 v[36:39], v11 offset:0
	ds_read_b128 v[44:47], v92 offset:0
	ds_read_b128 v[48:51], v92 offset:1024
	s_waitcnt lgkmcnt(0)
	v_mfma_f32_32x32x16_f16 v[96:111], v[32:35], v[28:31], 0
	v_mfma_f32_32x32x16_f16 v[128:143], v[36:39], v[44:47], 0
	v_mfma_f32_32x32x16_f16 v[160:175], v[36:39], v[48:51], 0
	ds_read_u16 v32, v9 offset:32
	ds_read_b128 v[36:39], v11 offset:256
	ds_read_b128 v[44:47], v92 offset:2048
	ds_read_b128 v[48:51], v92 offset:3072
	s_nop 15
	s_nop 15
.Lscan_loop:
	v_exp_f32_e32 v96, v96
	v_exp_f32_e32 v97, v97
	v_mfma_f32_16x16x32_f16 v[80:83], v[72:75], v[24:27], v[80:83]
	ds_read_b128 v[60:63], v92 offset:34816
	ds_bpermute_b32 v90, v87, v85
	s_waitcnt lgkmcnt(2)
	v_exp_f32_e32 v98, v98
	v_exp_f32_e32 v99, v99
	v_mfma_f32_32x32x16_f16 v[112:127], v[32:35], v[28:31], 0
	ds_read_u16 v32, v9 offset:64
	ds_read_b128 v[64:67], v92 offset:35840
	v_fmac_f32_e32 v128, v96, v191
	v_exp_f32_e32 v100, v100
	v_fmac_f32_e32 v129, v97, v128
	v_exp_f32_e32 v101, v101
	v_fmac_f32_e32 v130, v98, v129
	v_cvt_pkrtz_f16_f32 v68, v128, v129
	v_exp_f32_e32 v102, v102
	v_fmac_f32_e32 v131, v99, v130
	v_pk_mul_f16 v68, v52, v68
	v_exp_f32_e32 v103, v103
	v_add_f32_e32 v84, v80, v81
	v_add_f32_e32 v91, v82, v83
	v_fmac_f32_e32 v132, v100, v131
	v_add_f32_e32 v84, v84, v91
	v_cvt_pkrtz_f16_f32 v69, v130, v131
	v_mfma_f32_32x32x16_f16 v[144:159], v[36:39], v[44:47], 0
	ds_read_b128 v[44:47], v92 offset:4096
	ds_bpermute_b32 v89, v86, v84
	v_exp_f32_e32 v104, v104
	v_fmac_f32_e32 v133, v101, v132
	v_pk_mul_f16 v69, v53, v69
	v_exp_f32_e32 v105, v105
	v_fmac_f32_e32 v134, v102, v133
	v_cvt_pkrtz_f16_f32 v70, v132, v133
	v_exp_f32_e32 v106, v106
	v_fmac_f32_e32 v135, v103, v134
	v_pk_mul_f16 v70, v54, v70
	v_exp_f32_e32 v107, v107
	v_mfma_f32_32x32x16_f16 v[176:191], v[36:39], v[48:51], 0
	ds_read_b128 v[36:39], v11 offset:512
	ds_read_b128 v[48:51], v92 offset:5120
	v_cvt_pkrtz_f16_f32 v71, v134, v135
	v_fmac_f32_e32 v168, v104, v135
	v_pk_mul_f16 v71, v55, v71
	v_exp_f32_e32 v108, v108
	v_fmac_f32_e32 v169, v105, v168
	v_mfma_f32_16x16x32_f16 v[76:79], v[68:71], v[20:23], 0
	s_waitcnt lgkmcnt(2)
	v_add_f32_e32 v198, v85, v90
	v_cvt_pkrtz_f16_f32 v72, v168, v169
	v_exp_f32_e32 v109, v109
	v_fmac_f32_e32 v170, v106, v169
	v_add_f32_e32 v88, v84, v89
	v_pk_mul_f16 v72, v56, v72
	v_fmac_f32_e32 v171, v107, v170
	v_exp_f32_e32 v110, v110
	v_cvt_pkrtz_f16_f32 v73, v170, v171
	v_fmac_f32_e32 v172, v108, v171
	v_pk_mul_f16 v73, v57, v73
	v_fmac_f32_e32 v173, v109, v172
	v_exp_f32_e32 v111, v111
	v_cvt_pkrtz_f16_f32 v74, v172, v173
	v_fmac_f32_e32 v174, v110, v173
	v_pk_mul_f16 v74, v58, v74
	v_fmac_f32_e32 v175, v111, v174
	v_cvt_pkrtz_f16_f32 v75, v174, v175
	v_pk_mul_f16 v75, v59, v75
	v_exp_f32_e32 v112, v112
	v_exp_f32_e32 v113, v113
	v_mfma_f32_16x16x32_f16 v[76:79], v[72:75], v[24:27], v[76:79]
	ds_read_b128 v[52:55], v92 offset:36864
	ds_bpermute_b32 v90, v87, v88
	s_waitcnt lgkmcnt(2)
	v_exp_f32_e32 v114, v114
	v_exp_f32_e32 v115, v115
	v_mfma_f32_32x32x16_f16 v[96:111], v[32:35], v[28:31], 0
	ds_read_u16 v32, v9 offset:96
	ds_read_b128 v[56:59], v92 offset:37888
	v_fmac_f32_e32 v144, v112, v175
	v_exp_f32_e32 v116, v116
	v_fmac_f32_e32 v145, v113, v144
	v_exp_f32_e32 v117, v117
	v_fmac_f32_e32 v146, v114, v145
	v_cvt_pkrtz_f16_f32 v68, v144, v145
	v_exp_f32_e32 v118, v118
	v_fmac_f32_e32 v147, v115, v146
	v_pk_mul_f16 v68, v60, v68
	v_exp_f32_e32 v119, v119
	v_add_f32_e32 v84, v76, v77
	v_add_f32_e32 v91, v78, v79
	v_fmac_f32_e32 v148, v116, v147
	v_add_f32_e32 v84, v84, v91
	v_cvt_pkrtz_f16_f32 v69, v146, v147
	v_mfma_f32_32x32x16_f16 v[128:143], v[36:39], v[44:47], 0
	ds_read_b128 v[44:47], v92 offset:6144
	ds_bpermute_b32 v89, v86, v84
	v_exp_f32_e32 v120, v120
	v_fmac_f32_e32 v149, v117, v148
	v_pk_mul_f16 v69, v61, v69
	v_exp_f32_e32 v121, v121
	v_fmac_f32_e32 v150, v118, v149
	v_cvt_pkrtz_f16_f32 v70, v148, v149
	v_exp_f32_e32 v122, v122
	v_fmac_f32_e32 v151, v119, v150
	v_pk_mul_f16 v70, v62, v70
	v_exp_f32_e32 v123, v123
	v_mfma_f32_32x32x16_f16 v[160:175], v[36:39], v[48:51], 0
	ds_read_b128 v[36:39], v11 offset:768
	ds_read_b128 v[48:51], v92 offset:7168
	v_cvt_pkrtz_f16_f32 v71, v150, v151
	v_fmac_f32_e32 v184, v120, v151
	v_pk_mul_f16 v71, v63, v71
	v_exp_f32_e32 v124, v124
	v_fmac_f32_e32 v185, v121, v184
	v_mfma_f32_16x16x32_f16 v[80:83], v[68:71], v[20:23], 0
	s_waitcnt lgkmcnt(2)
	v_add_f32_e32 v199, v88, v90
	v_cvt_pkrtz_f16_f32 v72, v184, v185
	v_exp_f32_e32 v125, v125
	v_fmac_f32_e32 v186, v122, v185
	v_add_f32_e32 v85, v84, v89
	v_pk_mul_f16 v72, v64, v72
	v_fmac_f32_e32 v187, v123, v186
	v_exp_f32_e32 v126, v126
	v_cvt_pkrtz_f16_f32 v73, v186, v187
	v_fmac_f32_e32 v188, v124, v187
	v_pk_mul_f16 v73, v65, v73
	v_fmac_f32_e32 v189, v125, v188
	v_exp_f32_e32 v127, v127
	v_cvt_pkrtz_f16_f32 v74, v188, v189
	v_fmac_f32_e32 v190, v126, v189
	v_pk_mul_f16 v74, v66, v74
	v_fmac_f32_e32 v191, v127, v190
	v_cvt_pkrtz_f16_f32 v75, v190, v191
	v_pk_mul_f16 v75, v67, v75
	v_exp_f32_e32 v96, v96
	v_exp_f32_e32 v97, v97
	v_mfma_f32_16x16x32_f16 v[80:83], v[72:75], v[24:27], v[80:83]
	ds_read_b128 v[60:63], v92 offset:38912
	ds_bpermute_b32 v90, v87, v85
	s_waitcnt lgkmcnt(2)
	v_exp_f32_e32 v98, v98
	v_exp_f32_e32 v99, v99
	v_mfma_f32_32x32x16_f16 v[112:127], v[32:35], v[28:31], 0
	ds_read_u16 v32, v9 offset:128
	ds_read_b128 v[64:67], v92 offset:39936
	v_fmac_f32_e32 v128, v96, v191
	v_exp_f32_e32 v100, v100
	v_fmac_f32_e32 v129, v97, v128
	v_exp_f32_e32 v101, v101
	v_fmac_f32_e32 v130, v98, v129
	v_cvt_pkrtz_f16_f32 v68, v128, v129
	v_exp_f32_e32 v102, v102
	v_fmac_f32_e32 v131, v99, v130
	v_pk_mul_f16 v68, v52, v68
	v_exp_f32_e32 v103, v103
	v_add_f32_e32 v84, v80, v81
	v_add_f32_e32 v91, v82, v83
	v_fmac_f32_e32 v132, v100, v131
	v_add_f32_e32 v84, v84, v91
	v_cvt_pkrtz_f16_f32 v69, v130, v131
	v_mfma_f32_32x32x16_f16 v[144:159], v[36:39], v[44:47], 0
	ds_read_b128 v[44:47], v92 offset:8192
	ds_bpermute_b32 v89, v86, v84
	v_exp_f32_e32 v104, v104
	v_fmac_f32_e32 v133, v101, v132
	v_pk_mul_f16 v69, v53, v69
	v_exp_f32_e32 v105, v105
	v_fmac_f32_e32 v134, v102, v133
	v_cvt_pkrtz_f16_f32 v70, v132, v133
	v_exp_f32_e32 v106, v106
	v_fmac_f32_e32 v135, v103, v134
	v_pk_mul_f16 v70, v54, v70
	v_exp_f32_e32 v107, v107
	v_mfma_f32_32x32x16_f16 v[176:191], v[36:39], v[48:51], 0
	ds_read_b128 v[36:39], v11 offset:1024
	ds_read_b128 v[48:51], v92 offset:9216
	v_cvt_pkrtz_f16_f32 v71, v134, v135
	v_fmac_f32_e32 v168, v104, v135
	v_pk_mul_f16 v71, v55, v71
	v_exp_f32_e32 v108, v108
	v_fmac_f32_e32 v169, v105, v168
	v_mfma_f32_16x16x32_f16 v[76:79], v[68:71], v[20:23], 0
	s_waitcnt lgkmcnt(2)
	v_add_f32_e32 v192, v85, v90
	v_cvt_pkrtz_f16_f32 v72, v168, v169
	v_exp_f32_e32 v109, v109
	v_fmac_f32_e32 v170, v106, v169
	v_add_f32_e32 v88, v84, v89
	v_pk_mul_f16 v72, v56, v72
	v_fmac_f32_e32 v171, v107, v170
	v_exp_f32_e32 v110, v110
	v_cvt_pkrtz_f16_f32 v73, v170, v171
	v_fmac_f32_e32 v172, v108, v171
	v_pk_mul_f16 v73, v57, v73
	v_fmac_f32_e32 v173, v109, v172
	v_exp_f32_e32 v111, v111
	v_cvt_pkrtz_f16_f32 v74, v172, v173
	v_fmac_f32_e32 v174, v110, v173
	v_pk_mul_f16 v74, v58, v74
	v_fmac_f32_e32 v175, v111, v174
	v_cvt_pkrtz_f16_f32 v75, v174, v175
	v_pk_mul_f16 v75, v59, v75
	v_exp_f32_e32 v112, v112
	v_exp_f32_e32 v113, v113
	v_mfma_f32_16x16x32_f16 v[76:79], v[72:75], v[24:27], v[76:79]
	ds_read_b128 v[52:55], v92 offset:40960
	ds_bpermute_b32 v90, v87, v88
	s_waitcnt lgkmcnt(2)
	v_exp_f32_e32 v114, v114
	v_exp_f32_e32 v115, v115
	v_mfma_f32_32x32x16_f16 v[96:111], v[32:35], v[28:31], 0
	ds_read_u16 v32, v9 offset:160
	ds_read_b128 v[56:59], v92 offset:41984
	v_fmac_f32_e32 v144, v112, v175
	v_exp_f32_e32 v116, v116
	v_fmac_f32_e32 v145, v113, v144
	v_exp_f32_e32 v117, v117
	v_fmac_f32_e32 v146, v114, v145
	v_cvt_pkrtz_f16_f32 v68, v144, v145
	v_exp_f32_e32 v118, v118
	v_fmac_f32_e32 v147, v115, v146
	v_pk_mul_f16 v68, v60, v68
	v_exp_f32_e32 v119, v119
	v_add_f32_e32 v84, v76, v77
	v_add_f32_e32 v91, v78, v79
	v_fmac_f32_e32 v148, v116, v147
	v_add_f32_e32 v84, v84, v91
	v_cvt_pkrtz_f16_f32 v69, v146, v147
	v_mfma_f32_32x32x16_f16 v[128:143], v[36:39], v[44:47], 0
	ds_read_b128 v[44:47], v92 offset:10240
	ds_bpermute_b32 v89, v86, v84
	v_exp_f32_e32 v120, v120
	v_fmac_f32_e32 v149, v117, v148
	v_pk_mul_f16 v69, v61, v69
	v_exp_f32_e32 v121, v121
	v_fmac_f32_e32 v150, v118, v149
	v_cvt_pkrtz_f16_f32 v70, v148, v149
	v_exp_f32_e32 v122, v122
	v_fmac_f32_e32 v151, v119, v150
	v_pk_mul_f16 v70, v62, v70
	v_exp_f32_e32 v123, v123
	v_mfma_f32_32x32x16_f16 v[160:175], v[36:39], v[48:51], 0
	ds_read_b128 v[36:39], v11 offset:1280
	ds_read_b128 v[48:51], v92 offset:11264
	v_cvt_pkrtz_f16_f32 v71, v150, v151
	v_fmac_f32_e32 v184, v120, v151
	v_pk_mul_f16 v71, v63, v71
	v_exp_f32_e32 v124, v124
	v_fmac_f32_e32 v185, v121, v184
	v_mfma_f32_16x16x32_f16 v[80:83], v[68:71], v[20:23], 0
	s_waitcnt lgkmcnt(2)
	v_add_f32_e32 v193, v88, v90
	v_cvt_pkrtz_f16_f32 v72, v184, v185
	v_exp_f32_e32 v125, v125
	v_fmac_f32_e32 v186, v122, v185
	v_add_f32_e32 v85, v84, v89
	v_pk_mul_f16 v72, v64, v72
	v_fmac_f32_e32 v187, v123, v186
	v_exp_f32_e32 v126, v126
	v_cvt_pkrtz_f16_f32 v73, v186, v187
	v_fmac_f32_e32 v188, v124, v187
	v_pk_mul_f16 v73, v65, v73
	v_fmac_f32_e32 v189, v125, v188
	v_exp_f32_e32 v127, v127
	v_cvt_pkrtz_f16_f32 v74, v188, v189
	v_fmac_f32_e32 v190, v126, v189
	v_pk_mul_f16 v74, v66, v74
	v_fmac_f32_e32 v191, v127, v190
	v_cvt_pkrtz_f16_f32 v75, v190, v191
	v_pk_mul_f16 v75, v67, v75
	v_exp_f32_e32 v96, v96
	v_exp_f32_e32 v97, v97
	v_mfma_f32_16x16x32_f16 v[80:83], v[72:75], v[24:27], v[80:83]
	ds_read_b128 v[60:63], v92 offset:43008
	ds_bpermute_b32 v90, v87, v85
	s_waitcnt lgkmcnt(2)
	v_exp_f32_e32 v98, v98
	v_exp_f32_e32 v99, v99
	v_mfma_f32_32x32x16_f16 v[112:127], v[32:35], v[28:31], 0
	ds_read_u16 v32, v9 offset:192
	ds_read_b128 v[64:67], v92 offset:44032
	v_fmac_f32_e32 v128, v96, v191
	v_exp_f32_e32 v100, v100
	v_fmac_f32_e32 v129, v97, v128
	v_exp_f32_e32 v101, v101
	v_fmac_f32_e32 v130, v98, v129
	v_cvt_pkrtz_f16_f32 v68, v128, v129
	v_exp_f32_e32 v102, v102
	v_fmac_f32_e32 v131, v99, v130
	v_pk_mul_f16 v68, v52, v68
	v_exp_f32_e32 v103, v103
	v_add_f32_e32 v84, v80, v81
	v_add_f32_e32 v91, v82, v83
	v_fmac_f32_e32 v132, v100, v131
	v_add_f32_e32 v84, v84, v91
	v_cvt_pkrtz_f16_f32 v69, v130, v131
	v_mfma_f32_32x32x16_f16 v[144:159], v[36:39], v[44:47], 0
	ds_read_b128 v[44:47], v92 offset:12288
	ds_bpermute_b32 v89, v86, v84
	v_exp_f32_e32 v104, v104
	v_fmac_f32_e32 v133, v101, v132
	v_pk_mul_f16 v69, v53, v69
	v_exp_f32_e32 v105, v105
	v_fmac_f32_e32 v134, v102, v133
	v_cvt_pkrtz_f16_f32 v70, v132, v133
	v_exp_f32_e32 v106, v106
	v_fmac_f32_e32 v135, v103, v134
	v_pk_mul_f16 v70, v54, v70
	v_exp_f32_e32 v107, v107
	v_mfma_f32_32x32x16_f16 v[176:191], v[36:39], v[48:51], 0
	ds_read_b128 v[36:39], v11 offset:1536
	ds_read_b128 v[48:51], v92 offset:13312
	v_cvt_pkrtz_f16_f32 v71, v134, v135
	v_fmac_f32_e32 v168, v104, v135
	v_pk_mul_f16 v71, v55, v71
	v_exp_f32_e32 v108, v108
	v_fmac_f32_e32 v169, v105, v168
	v_mfma_f32_16x16x32_f16 v[76:79], v[68:71], v[20:23], 0
	s_waitcnt lgkmcnt(2)
	v_add_f32_e32 v194, v85, v90
	v_cvt_pkrtz_f16_f32 v72, v168, v169
	v_exp_f32_e32 v109, v109
	v_fmac_f32_e32 v170, v106, v169
	v_add_f32_e32 v88, v84, v89
	v_pk_mul_f16 v72, v56, v72
	v_fmac_f32_e32 v171, v107, v170
	v_exp_f32_e32 v110, v110
	v_cvt_pkrtz_f16_f32 v73, v170, v171
	v_fmac_f32_e32 v172, v108, v171
	v_pk_mul_f16 v73, v57, v73
	v_fmac_f32_e32 v173, v109, v172
	v_exp_f32_e32 v111, v111
	v_cvt_pkrtz_f16_f32 v74, v172, v173
	v_fmac_f32_e32 v174, v110, v173
	v_pk_mul_f16 v74, v58, v74
	v_fmac_f32_e32 v175, v111, v174
	v_cvt_pkrtz_f16_f32 v75, v174, v175
	v_pk_mul_f16 v75, v59, v75
	v_exp_f32_e32 v112, v112
	v_exp_f32_e32 v113, v113
	v_mfma_f32_16x16x32_f16 v[76:79], v[72:75], v[24:27], v[76:79]
	ds_read_b128 v[52:55], v92 offset:45056
	ds_bpermute_b32 v90, v87, v88
	s_waitcnt lgkmcnt(2)
	v_exp_f32_e32 v114, v114
	v_exp_f32_e32 v115, v115
	v_mfma_f32_32x32x16_f16 v[96:111], v[32:35], v[28:31], 0
	ds_read_u16 v32, v9 offset:224
	ds_read_b128 v[56:59], v92 offset:46080
	v_fmac_f32_e32 v144, v112, v175
	v_exp_f32_e32 v116, v116
	v_fmac_f32_e32 v145, v113, v144
	v_exp_f32_e32 v117, v117
	v_fmac_f32_e32 v146, v114, v145
	v_cvt_pkrtz_f16_f32 v68, v144, v145
	v_exp_f32_e32 v118, v118
	v_fmac_f32_e32 v147, v115, v146
	v_pk_mul_f16 v68, v60, v68
	v_exp_f32_e32 v119, v119
	v_add_f32_e32 v84, v76, v77
	v_add_f32_e32 v91, v78, v79
	v_fmac_f32_e32 v148, v116, v147
	v_add_f32_e32 v84, v84, v91
	v_cvt_pkrtz_f16_f32 v69, v146, v147
	v_mfma_f32_32x32x16_f16 v[128:143], v[36:39], v[44:47], 0
	ds_read_b128 v[44:47], v92 offset:14336
	ds_bpermute_b32 v89, v86, v84
	v_exp_f32_e32 v120, v120
	v_fmac_f32_e32 v149, v117, v148
	v_pk_mul_f16 v69, v61, v69
	v_exp_f32_e32 v121, v121
	v_fmac_f32_e32 v150, v118, v149
	v_cvt_pkrtz_f16_f32 v70, v148, v149
	v_exp_f32_e32 v122, v122
	v_fmac_f32_e32 v151, v119, v150
	v_pk_mul_f16 v70, v62, v70
	v_exp_f32_e32 v123, v123
	v_mfma_f32_32x32x16_f16 v[160:175], v[36:39], v[48:51], 0
	ds_read_b128 v[36:39], v11 offset:1792
	ds_read_b128 v[48:51], v92 offset:15360
	v_cvt_pkrtz_f16_f32 v71, v150, v151
	v_fmac_f32_e32 v184, v120, v151
	v_pk_mul_f16 v71, v63, v71
	v_exp_f32_e32 v124, v124
	v_fmac_f32_e32 v185, v121, v184
	v_mfma_f32_16x16x32_f16 v[80:83], v[68:71], v[20:23], 0
	s_waitcnt lgkmcnt(2)
	v_add_f32_e32 v195, v88, v90
	v_cvt_pkrtz_f16_f32 v72, v184, v185
	v_exp_f32_e32 v125, v125
	v_fmac_f32_e32 v186, v122, v185
	v_add_f32_e32 v85, v84, v89
	v_pk_mul_f16 v72, v64, v72
	v_fmac_f32_e32 v187, v123, v186
	v_exp_f32_e32 v126, v126
	v_cvt_pkrtz_f16_f32 v73, v186, v187
	v_fmac_f32_e32 v188, v124, v187
	v_pk_mul_f16 v73, v65, v73
	v_fmac_f32_e32 v189, v125, v188
	v_exp_f32_e32 v127, v127
	v_cvt_pkrtz_f16_f32 v74, v188, v189
	v_fmac_f32_e32 v190, v126, v189
	v_pk_mul_f16 v74, v66, v74
	v_fmac_f32_e32 v191, v127, v190
	v_cvt_pkrtz_f16_f32 v75, v190, v191
	v_pk_mul_f16 v75, v67, v75
	v_exp_f32_e32 v96, v96
	v_exp_f32_e32 v97, v97
	v_mfma_f32_16x16x32_f16 v[80:83], v[72:75], v[24:27], v[80:83]
	ds_read_b128 v[60:63], v92 offset:47104
	ds_read_b128 v[64:67], v92 offset:48128
	ds_bpermute_b32 v90, v87, v85
	s_waitcnt vmcnt(0)
	ds_write_b16 v94, v18
	ds_write_b16 v94, v19 offset:1024
	s_waitcnt lgkmcnt(0)
	s_barrier
	v_exp_f32_e32 v98, v98
	v_exp_f32_e32 v99, v99
	v_mfma_f32_32x32x16_f16 v[112:127], v[32:35], v[28:31], 0
	s_mov_b32 m0, s32
	ds_read_u16 v32, v10 offset:0
	global_load_lds_dwordx4 v2, s[20:21]
	v_fmac_f32_e32 v128, v96, v191
	v_exp_f32_e32 v100, v100
	v_fmac_f32_e32 v129, v97, v128
	v_exp_f32_e32 v101, v101
	v_fmac_f32_e32 v130, v98, v129
	v_cvt_pkrtz_f16_f32 v68, v128, v129
	v_exp_f32_e32 v102, v102
	v_fmac_f32_e32 v131, v99, v130
	v_pk_mul_f16 v68, v52, v68
	v_exp_f32_e32 v103, v103
	v_add_f32_e32 v84, v80, v81
	v_add_f32_e32 v91, v82, v83
	v_fmac_f32_e32 v132, v100, v131
	v_add_f32_e32 v84, v84, v91
	v_cvt_pkrtz_f16_f32 v69, v130, v131
	v_mfma_f32_32x32x16_f16 v[144:159], v[36:39], v[44:47], 0
	ds_read_b128 v[44:47], v93 offset:0
	ds_bpermute_b32 v89, v86, v84
	s_add_i32 m0, s32, 32768
	s_nop 0
	global_load_lds_dwordx4 v2, s[22:23]
	v_exp_f32_e32 v104, v104
	v_fmac_f32_e32 v133, v101, v132
	v_pk_mul_f16 v69, v53, v69
	v_exp_f32_e32 v105, v105
	v_fmac_f32_e32 v134, v102, v133
	v_cvt_pkrtz_f16_f32 v70, v132, v133
	v_exp_f32_e32 v106, v106
	v_fmac_f32_e32 v135, v103, v134
	v_pk_mul_f16 v70, v54, v70
	v_exp_f32_e32 v107, v107
	v_mfma_f32_32x32x16_f16 v[176:191], v[36:39], v[48:51], 0
	ds_read_b128 v[36:39], v13 offset:0
	s_mov_b32 m0, s33
	ds_read_b128 v[48:51], v93 offset:1024
	global_load_lds_dwordx4 v3, s[20:21]
	v_cvt_pkrtz_f16_f32 v71, v134, v135
	v_fmac_f32_e32 v168, v104, v135
	v_pk_mul_f16 v71, v55, v71
	v_exp_f32_e32 v108, v108
	v_fmac_f32_e32 v169, v105, v168
	v_mfma_f32_16x16x32_f16 v[76:79], v[68:71], v[20:23], 0
	s_waitcnt lgkmcnt(2)
	s_add_i32 m0, s33, 32768
	s_nop 0
	global_load_lds_dwordx4 v3, s[22:23]
	v_add_f32_e32 v196, v85, v90
	v_cvt_pkrtz_f16_f32 v72, v168, v169
	v_exp_f32_e32 v109, v109
	v_fmac_f32_e32 v170, v106, v169
	v_add_f32_e32 v88, v84, v89
	v_pk_mul_f16 v72, v56, v72
	v_fmac_f32_e32 v171, v107, v170
	v_exp_f32_e32 v110, v110
	v_cvt_pkrtz_f16_f32 v73, v170, v171
	v_fmac_f32_e32 v172, v108, v171
	v_pk_mul_f16 v73, v57, v73
	v_fmac_f32_e32 v173, v109, v172
	v_exp_f32_e32 v111, v111
	v_cvt_pkrtz_f16_f32 v74, v172, v173
	v_fmac_f32_e32 v174, v110, v173
	v_pk_mul_f16 v74, v58, v74
	v_fmac_f32_e32 v175, v111, v174
	v_cvt_pkrtz_f16_f32 v75, v174, v175
	v_pk_mul_f16 v75, v59, v75
	v_exp_f32_e32 v112, v112
	v_exp_f32_e32 v113, v113
	v_mfma_f32_16x16x32_f16 v[76:79], v[72:75], v[24:27], v[76:79]
	s_mov_b32 m0, s34
	ds_read_b128 v[52:55], v93 offset:32768
	global_load_lds_dwordx4 v4, s[20:21]
	ds_bpermute_b32 v90, v87, v88
	s_waitcnt lgkmcnt(2)
	v_exp_f32_e32 v114, v114
	v_exp_f32_e32 v115, v115
	v_mfma_f32_32x32x16_f16 v[96:111], v[32:35], v[28:31], 0
	ds_read_u16 v32, v10 offset:32
	s_add_i32 m0, s34, 32768
	ds_read_b128 v[56:59], v93 offset:33792
	global_load_lds_dwordx4 v4, s[22:23]
	v_fmac_f32_e32 v144, v112, v175
	v_exp_f32_e32 v116, v116
	v_fmac_f32_e32 v145, v113, v144
	v_exp_f32_e32 v117, v117
	v_fmac_f32_e32 v146, v114, v145
	v_cvt_pkrtz_f16_f32 v68, v144, v145
	v_exp_f32_e32 v118, v118
	v_fmac_f32_e32 v147, v115, v146
	v_pk_mul_f16 v68, v60, v68
	v_exp_f32_e32 v119, v119
	v_add_f32_e32 v84, v76, v77
	v_add_f32_e32 v91, v78, v79
	v_fmac_f32_e32 v148, v116, v147
	v_add_f32_e32 v84, v84, v91
	v_cvt_pkrtz_f16_f32 v69, v146, v147
	v_mfma_f32_32x32x16_f16 v[128:143], v[36:39], v[44:47], 0
	ds_read_b128 v[44:47], v93 offset:2048
	ds_bpermute_b32 v89, v86, v84
	s_cmp_eq_u32 s40, 0
	s_cselect_b64 s[56:57], 0, s[42:43]
	s_and_saveexec_b64 s[44:45], s[56:57]
	global_store_dword v[16:17], v197, off offset:-192
	global_store_dword v[16:17], v198, off offset:-128
	global_store_dword v[16:17], v199, off offset:-64
	s_and_b64 exec, s[44:45], s[42:43]
	global_store_dword v[16:17], v192, off
	global_store_dword v[16:17], v193, off offset:64
	global_store_dword v[16:17], v194, off offset:128
	global_store_dword v[16:17], v195, off offset:192
	global_store_dword v[16:17], v196, off offset:256
	s_mov_b64 exec, s[44:45]
	v_exp_f32_e32 v120, v120
	v_fmac_f32_e32 v149, v117, v148
	v_pk_mul_f16 v69, v61, v69
	v_exp_f32_e32 v121, v121
	v_fmac_f32_e32 v150, v118, v149
	v_cvt_pkrtz_f16_f32 v70, v148, v149
	v_exp_f32_e32 v122, v122
	v_fmac_f32_e32 v151, v119, v150
	v_pk_mul_f16 v70, v62, v70
	v_exp_f32_e32 v123, v123
	v_mfma_f32_32x32x16_f16 v[160:175], v[36:39], v[48:51], 0
	ds_read_b128 v[36:39], v13 offset:256
	s_mov_b32 m0, s35
	ds_read_b128 v[48:51], v93 offset:3072
	global_load_lds_dwordx4 v5, s[20:21]
	s_add_i32 m0, s35, 32768
	s_nop 0
	global_load_lds_dwordx4 v5, s[22:23]
	v_cvt_pkrtz_f16_f32 v71, v150, v151
	v_fmac_f32_e32 v184, v120, v151
	v_pk_mul_f16 v71, v63, v71
	v_exp_f32_e32 v124, v124
	v_fmac_f32_e32 v185, v121, v184
	v_mfma_f32_16x16x32_f16 v[80:83], v[68:71], v[20:23], 0
	s_waitcnt lgkmcnt(2)
	s_mov_b32 m0, s29
	s_nop 0
	global_load_lds_dword v6, s[24:25]
	global_load_ushort v18, v7, s[26:27]
	global_load_ushort v19, v7, s[26:27] offset:128
	v_add_f32_e32 v197, v88, v90
	v_cvt_pkrtz_f16_f32 v72, v184, v185
	v_exp_f32_e32 v125, v125
	v_fmac_f32_e32 v186, v122, v185
	v_add_f32_e32 v85, v84, v89
	v_pk_mul_f16 v72, v64, v72
	v_fmac_f32_e32 v187, v123, v186
	v_exp_f32_e32 v126, v126
	v_cvt_pkrtz_f16_f32 v73, v186, v187
	v_fmac_f32_e32 v188, v124, v187
	v_pk_mul_f16 v73, v65, v73
	v_fmac_f32_e32 v189, v125, v188
	v_exp_f32_e32 v127, v127
	v_cvt_pkrtz_f16_f32 v74, v188, v189
	v_fmac_f32_e32 v190, v126, v189
	v_pk_mul_f16 v74, v66, v74
	v_fmac_f32_e32 v191, v127, v190
	v_cvt_pkrtz_f16_f32 v75, v190, v191
	s_cmp_lt_u32 s40, 29
	s_cselect_b32 s58, 0x4000, 0
	s_cselect_b32 s59, 0x100, 0
	s_add_u32 s20, s20, s58
	s_addc_u32 s21, s21, 0
	s_add_u32 s22, s22, s58
	s_addc_u32 s23, s23, 0
	s_add_u32 s24, s24, s59
	s_addc_u32 s25, s25, 0
	s_add_u32 s26, s26, s59
	s_addc_u32 s27, s27, 0
	v_pk_mul_f16 v75, v67, v75
	v_lshl_add_u64 v[16:17], v[16:17], 0, s[46:47]
	v_swap_b32 v92, v93
	v_swap_b32 v9, v10
	v_swap_b32 v11, v13
	v_swap_b32 v8, v94
	s_xor_b32 s32, s32, 0x4000
	s_xor_b32 s33, s33, 0x4000
	s_xor_b32 s34, s34, 0x4000
	s_xor_b32 s35, s35, 0x4000
	s_xor_b32 s29, s29, 0x100
	s_add_u32 s40, s40, 1
	s_cmp_lt_u32 s40, 32
	s_cbranch_scc1 .Lscan_loop
	s_nop 1
	v_mfma_f32_16x16x32_f16 v[80:83], v[72:75], v[24:27], v[80:83]
	ds_bpermute_b32 v90, v87, v85
	s_nop 15
	v_add_f32_e32 v84, v80, v81
	v_add_f32_e32 v91, v82, v83
	s_nop 0
	v_add_f32_e32 v84, v84, v91
	s_waitcnt lgkmcnt(0)
	v_add_f32_e32 v198, v85, v90
	ds_bpermute_b32 v89, v86, v84
	s_waitcnt lgkmcnt(0)
	v_add_f32_e32 v88, v84, v89
	s_nop 0
	ds_bpermute_b32 v90, v87, v88
	s_waitcnt lgkmcnt(0)
	v_add_f32_e32 v199, v88, v90
	s_nop 1
	s_and_saveexec_b64 s[44:45], s[42:43]
	global_store_dword v[16:17], v197, off offset:-192
	global_store_dword v[16:17], v198, off offset:-128
	global_store_dword v[16:17], v199, off offset:-64
	s_waitcnt vmcnt(0)
	s_endpgm

	.amdhsa_kernel _Z6scan_kPKDF16_S0_S0_S0_PKfPf
		.amdhsa_group_segment_fixed_size 86016
		.amdhsa_private_segment_fixed_size 0
		.amdhsa_kernarg_size 48
		.amdhsa_user_sgpr_count 2
		.amdhsa_user_sgpr_dispatch_ptr 0
		.amdhsa_user_sgpr_queue_ptr 0
		.amdhsa_user_sgpr_kernarg_segment_ptr 1
		.amdhsa_user_sgpr_dispatch_id 0
		.amdhsa_user_sgpr_kernarg_preload_length 0
		.amdhsa_user_sgpr_kernarg_preload_offset 0
		.amdhsa_user_sgpr_private_segment_size 0
		.amdhsa_uses_dynamic_stack 0
		.amdhsa_enable_private_segment 0
		.amdhsa_system_sgpr_workgroup_id_x 1
		.amdhsa_system_sgpr_workgroup_id_y 0
		.amdhsa_system_sgpr_workgroup_id_z 0
		.amdhsa_system_sgpr_workgroup_info 0
		.amdhsa_system_vgpr_workitem_id 0
		.amdhsa_next_free_vgpr 200
		.amdhsa_next_free_sgpr 96
		.amdhsa_accum_offset 200
		.amdhsa_reserve_vcc 1
		.amdhsa_float_round_mode_32 0
		.amdhsa_float_round_mode_16_64 0
		.amdhsa_float_denorm_mode_32 3
		.amdhsa_float_denorm_mode_16_64 3
		.amdhsa_dx10_clamp 1
		.amdhsa_ieee_mode 1
		.amdhsa_fp16_overflow 0
		.amdhsa_tg_split 0
		.amdhsa_exception_fp_ieee_invalid_op 0
		.amdhsa_exception_fp_denorm_src 0
		.amdhsa_exception_fp_ieee_div_zero 0
		.amdhsa_exception_fp_ieee_overflow 0
		.amdhsa_exception_fp_ieee_underflow 0
		.amdhsa_exception_fp_ieee_inexact 0
		.amdhsa_exception_int_div_zero 0
	.end_amdhsa_kernel

_Z6gemm_gILi32ELi64ELi16ELi32ELi1ELi1ELi64ELi4EEv5GemmP:
	s_load_dwordx8 s[4:11], s[0:1], 0x0
	s_load_dwordx2 s[12:13], s[0:1], 0x20
	s_load_dwordx2 s[14:15], s[0:1], 0x68
	v_lshrrev_b32_e32 v74, 6, v0
	v_lshrrev_b32_e32 v75, 3, v0
	v_readfirstlane_b32 s16, v74
	s_lshl_b32 s17, s2, 5
	s_lshl_b32 s18, s16, 10
	v_and_b32_e32 v76, 7, v0
	v_and_b32_e32 v77, 7, v75
	v_xor_b32_e32 v76, v76, v77
	v_lshlrev_b32_e32 v76, 4, v76
	v_add_u32_e32 v78, s17, v75
	v_bfe_u32 v79, v78, 6, 6
	v_and_b32_e32 v80, 63, v78
	v_lshl_add_u32 v82, v78, 8, v76
	v_mov_b32_e32 v83, 0
	v_mov_b32_e32 v77, 0
	s_waitcnt lgkmcnt(0)
	v_lshl_add_u64 v[84:85], s[4:5], 0, v[82:83]
	v_lshl_add_u64 v[86:87], s[14:15], 0, v[76:77]
	v_mul_u32_u24_e32 v58, 0x900, v75
	v_add_u32_e32 v58, v58, v76
	v_add_u32_e32 v59, 0x12000, v58
	s_mov_b32 s30, s6
	s_mov_b32 s31, s7
	s_mov_b32 s26, 0x80
	s_mov_b32 s27, 0
	v_add_u32_e32 v106, -1, v79
	v_add_u32_e32 v107, -1, v80
	v_max_u32_e32 v106, v106, v107
	s_mov_b32 s20, 4294950656
	s_mov_b32 s21, 4294967295
	v_cmp_gt_u32_e32 vcc, 64, v106
	v_lshl_add_u64 v[90:91], v[84:85], 0, s[20:21]
	s_nop 0
	v_cndmask_b32_e32 v110, v86, v90, vcc
	v_cndmask_b32_e32 v111, v87, v91, vcc
	v_lshl_add_u64 v[112:113], v[110:111], 0, s[26:27]
	v_add_u32_e32 v106, -1, v79
	v_add_u32_e32 v107, 0, v80
	v_max_u32_e32 v106, v106, v107
	s_mov_b32 s20, 4294950912
	s_mov_b32 s21, 4294967295
	v_cmp_gt_u32_e32 vcc, 64, v106
	v_lshl_add_u64 v[90:91], v[84:85], 0, s[20:21]
	s_nop 0
	v_cndmask_b32_e32 v114, v86, v90, vcc
	v_cndmask_b32_e32 v115, v87, v91, vcc
	v_lshl_add_u64 v[116:117], v[114:115], 0, s[26:27]
	v_add_u32_e32 v106, -1, v79
	v_add_u32_e32 v107, 1, v80
	v_max_u32_e32 v106, v106, v107
	s_mov_b32 s20, 4294951168
	s_mov_b32 s21, 4294967295
	v_cmp_gt_u32_e32 vcc, 64, v106
	v_lshl_add_u64 v[90:91], v[84:85], 0, s[20:21]
	s_nop 0
	v_cndmask_b32_e32 v118, v86, v90, vcc
	v_cndmask_b32_e32 v119, v87, v91, vcc
	v_lshl_add_u64 v[120:121], v[118:119], 0, s[26:27]
	v_add_u32_e32 v106, 0, v79
	v_add_u32_e32 v107, -1, v80
	v_max_u32_e32 v106, v106, v107
	s_mov_b32 s20, 4294967040
	s_mov_b32 s21, 4294967295
	v_cmp_gt_u32_e32 vcc, 64, v106
	v_lshl_add_u64 v[90:91], v[84:85], 0, s[20:21]
	s_nop 0
	v_cndmask_b32_e32 v122, v86, v90, vcc
	v_cndmask_b32_e32 v123, v87, v91, vcc
	v_lshl_add_u64 v[124:125], v[122:123], 0, s[26:27]
	v_add_u32_e32 v106, 0, v79
	v_add_u32_e32 v107, 0, v80
	v_max_u32_e32 v106, v106, v107
	s_mov_b32 s20, 0
	s_mov_b32 s21, 0
	v_cmp_gt_u32_e32 vcc, 64, v106
	v_lshl_add_u64 v[90:91], v[84:85], 0, s[20:21]
	s_nop 0
	v_cndmask_b32_e32 v126, v86, v90, vcc
	v_cndmask_b32_e32 v127, v87, v91, vcc
	v_lshl_add_u64 v[128:129], v[126:127], 0, s[26:27]
	v_add_u32_e32 v106, 0, v79
	v_add_u32_e32 v107, 1, v80
	v_max_u32_e32 v106, v106, v107
	s_mov_b32 s20, 256
	s_mov_b32 s21, 0
	v_cmp_gt_u32_e32 vcc, 64, v106
	v_lshl_add_u64 v[90:91], v[84:85], 0, s[20:21]
	s_nop 0
	v_cndmask_b32_e32 v130, v86, v90, vcc
	v_cndmask_b32_e32 v131, v87, v91, vcc
	v_lshl_add_u64 v[132:133], v[130:131], 0, s[26:27]
	v_add_u32_e32 v106, 1, v79
	v_add_u32_e32 v107, -1, v80
	v_max_u32_e32 v106, v106, v107
	s_mov_b32 s20, 16128
	s_mov_b32 s21, 0
	v_cmp_gt_u32_e32 vcc, 64, v106
	v_lshl_add_u64 v[90:91], v[84:85], 0, s[20:21]
	s_nop 0
	v_cndmask_b32_e32 v134, v86, v90, vcc
	v_cndmask_b32_e32 v135, v87, v91, vcc
	v_lshl_add_u64 v[136:137], v[134:135], 0, s[26:27]
	v_add_u32_e32 v106, 1, v79
	v_add_u32_e32 v107, 0, v80
	v_max_u32_e32 v106, v106, v107
	s_mov_b32 s20, 16384
	s_mov_b32 s21, 0
	v_cmp_gt_u32_e32 vcc, 64, v106
	v_lshl_add_u64 v[90:91], v[84:85], 0, s[20:21]
	s_nop 0
	v_cndmask_b32_e32 v138, v86, v90, vcc
	v_cndmask_b32_e32 v139, v87, v91, vcc
	v_lshl_add_u64 v[140:141], v[138:139], 0, s[26:27]
	v_add_u32_e32 v106, 1, v79
	v_add_u32_e32 v107, 1, v80
	v_max_u32_e32 v106, v106, v107
	s_mov_b32 s20, 16640
	s_mov_b32 s21, 0
	v_cmp_gt_u32_e32 vcc, 64, v106
	v_lshl_add_u64 v[90:91], v[84:85], 0, s[20:21]
	s_nop 0
	v_cndmask_b32_e32 v142, v86, v90, vcc
	v_cndmask_b32_e32 v143, v87, v91, vcc
	v_lshl_add_u64 v[144:145], v[142:143], 0, s[26:27]
	v_lshlrev_b32_e32 v92, 7, v78
	v_and_b32_e32 v93, 7, v0
	v_lshl_add_u32 v92, v93, 4, v92
	v_mov_b32_e32 v93, 0
	v_lshl_add_u64 v[94:95], s[10:11], 0, v[92:93]
	v_lshl_add_u64 v[96:97], s[12:13], 0, v[92:93]
	global_load_dwordx4 v[70:73], v[94:95], off
	v_and_b32_e32 v1, 15, v0
	v_bfe_u32 v2, v0, 4, 2
	s_lshr_b32 s22, s16, 1
	s_lshl_b32 s22, s22, 4
	s_and_b32 s23, s16, 1
	s_lshl_b32 s23, s23, 5
	v_and_b32_e32 v98, 7, v1
	v_xor_b32_e32 v98, v98, v2
	v_xor_b32_e32 v99, 4, v98
	v_lshlrev_b32_e32 v98, 4, v98
	v_lshlrev_b32_e32 v99, 4, v99
	v_add_u32_e32 v100, s22, v1
	v_lshlrev_b32_e32 v100, 7, v100
	v_add_u32_e32 v101, s23, v1
	v_lshlrev_b32_e32 v101, 7, v101
	v_add_u32_e32 v101, 0x1000, v101
	v_add_u32_e32 v62, v100, v98
	v_add_u32_e32 v63, v100, v99
	v_add_u32_e32 v66, v101, v98
	v_add_u32_e32 v67, v101, v99
	v_add_u32_e32 v64, 0xc000, v62
	v_add_u32_e32 v68, 0xc000, v66
	v_add_u32_e32 v65, 0xc000, v63
	v_add_u32_e32 v69, 0xc000, v67
	v_add_u32_e32 v102, s23, v1
	v_lshlrev_b32_e32 v102, 2, v102
	global_load_dword v36, v102, s[8:9]
	global_load_dword v37, v102, s[8:9] offset:64
	v_mov_b32_e32 v28, 0
	v_mov_b32_e32 v29, 0
	v_mov_b32_e32 v30, 0
	v_mov_b32_e32 v31, 0
	v_mov_b32_e32 v32, 0
	v_mov_b32_e32 v33, 0
	v_mov_b32_e32 v34, 0
	v_mov_b32_e32 v35, 0
	s_mov_b32 m0, s18
	s_nop 0
	global_load_lds_dwordx4 v[110:111], off
	s_add_i32 m0, s18, 4096
	s_nop 0
	global_load_lds_dwordx4 v58, s[30:31]
	s_add_i32 m0, s18, 8192
	s_nop 0
	global_load_lds_dwordx4 v59, s[30:31]
	s_add_u32 s30, s30, 0x80
	s_addc_u32 s31, s31, 0
	s_add_i32 m0, s18, 12288
	s_nop 0
	global_load_lds_dwordx4 v[112:113], off
	s_add_i32 m0, s18, 16384
	s_nop 0
	global_load_lds_dwordx4 v58, s[30:31]
	s_add_i32 m0, s18, 20480
	s_nop 0
	global_load_lds_dwordx4 v59, s[30:31]
	s_add_u32 s30, s30, 0x80
	s_addc_u32 s31, s31, 0
	s_add_i32 m0, s18, 24576
	s_nop 0
	global_load_lds_dwordx4 v[114:115], off
	s_add_i32 m0, s18, 28672
	s_nop 0
	global_load_lds_dwordx4 v58, s[30:31]
	s_add_i32 m0, s18, 32768
	s_nop 0
	global_load_lds_dwordx4 v59, s[30:31]
	s_add_u32 s30, s30, 0x80
	s_addc_u32 s31, s31, 0
	s_add_i32 m0, s18, 36864
	s_nop 0
	global_load_lds_dwordx4 v[116:117], off
	s_add_i32 m0, s18, 40960
	s_nop 0
	global_load_lds_dwordx4 v58, s[30:31]
	s_add_i32 m0, s18, 45056
	s_nop 0
	global_load_lds_dwordx4 v59, s[30:31]
	s_add_u32 s30, s30, 0x80
	s_addc_u32 s31, s31, 0
	s_add_i32 m0, s18, 49152
	s_nop 0
	global_load_lds_dwordx4 v[118:119], off
	s_add_i32 m0, s18, 53248
	s_nop 0
	global_load_lds_dwordx4 v58, s[30:31]
	s_add_i32 m0, s18, 57344
	s_nop 0
	global_load_lds_dwordx4 v59, s[30:31]
	s_add_u32 s30, s30, 0x80
	s_addc_u32 s31, s31, 0
	s_add_i32 m0, s18, 61440
	s_nop 0
	global_load_lds_dwordx4 v[120:121], off
	s_add_i32 m0, s18, 65536
	s_nop 0
	global_load_lds_dwordx4 v58, s[30:31]
	s_add_i32 m0, s18, 69632
	s_nop 0
	global_load_lds_dwordx4 v59, s[30:31]
	s_add_u32 s30, s30, 0x80
	s_addc_u32 s31, s31, 0
	s_add_i32 m0, s18, 73728
	s_nop 0
	global_load_lds_dwordx4 v[122:123], off
	s_add_i32 m0, s18, 77824
	s_nop 0
	global_load_lds_dwordx4 v58, s[30:31]
	s_add_i32 m0, s18, 81920
	s_nop 0
	global_load_lds_dwordx4 v59, s[30:31]
	s_add_u32 s30, s30, 0x80
	s_addc_u32 s31, s31, 0
	s_waitcnt vmcnt(18)
	s_barrier
	s_add_i32 m0, s18, 86016
	ds_read_b128 v[4:7], v62
	global_load_lds_dwordx4 v[124:125], off
	s_add_i32 m0, s18, 90112
	ds_read_b128 v[8:11], v66
	global_load_lds_dwordx4 v58, s[30:31]
	s_add_i32 m0, s18, 94208
	ds_read_b128 v[12:15], v66 offset:2048
	global_load_lds_dwordx4 v59, s[30:31]
	s_add_u32 s30, s30, 0x80
	s_addc_u32 s31, s31, 0
	ds_read_b128 v[16:19], v63
	ds_read_b128 v[20:23], v67
	ds_read_b128 v[24:27], v67 offset:2048
	s_waitcnt lgkmcnt(3)
	v_mfma_f32_16x16x32_f16 v[28:31], v[4:7], v[8:11], v[28:31]
	v_mfma_f32_16x16x32_f16 v[32:35], v[4:7], v[12:15], v[32:35]
	s_waitcnt lgkmcnt(0)
	v_mfma_f32_16x16x32_f16 v[28:31], v[16:19], v[20:23], v[28:31]
	v_mfma_f32_16x16x32_f16 v[32:35], v[16:19], v[24:27], v[32:35]
	s_waitcnt vmcnt(18)
	s_barrier
	s_mov_b32 m0, s18
	ds_read_b128 v[4:7], v62 offset:12288
	global_load_lds_dwordx4 v[126:127], off
	s_add_i32 m0, s18, 4096
	ds_read_b128 v[8:11], v66 offset:12288
	global_load_lds_dwordx4 v58, s[30:31]
	s_add_i32 m0, s18, 8192
	ds_read_b128 v[12:15], v66 offset:14336
	global_load_lds_dwordx4 v59, s[30:31]
	s_add_u32 s30, s30, 0x80
	s_addc_u32 s31, s31, 0
	ds_read_b128 v[16:19], v63 offset:12288
	ds_read_b128 v[20:23], v67 offset:12288
	ds_read_b128 v[24:27], v67 offset:14336
	s_waitcnt lgkmcnt(3)
	v_mfma_f32_16x16x32_f16 v[28:31], v[4:7], v[8:11], v[28:31]
	v_mfma_f32_16x16x32_f16 v[32:35], v[4:7], v[12:15], v[32:35]
	s_waitcnt lgkmcnt(0)
	v_mfma_f32_16x16x32_f16 v[28:31], v[16:19], v[20:23], v[28:31]
	v_mfma_f32_16x16x32_f16 v[32:35], v[16:19], v[24:27], v[32:35]
	s_waitcnt vmcnt(18)
	s_barrier
	s_add_i32 m0, s18, 12288
	ds_read_b128 v[4:7], v62 offset:24576
	global_load_lds_dwordx4 v[128:129], off
	s_add_i32 m0, s18, 16384
	ds_read_b128 v[8:11], v66 offset:24576
	global_load_lds_dwordx4 v58, s[30:31]
	s_add_i32 m0, s18, 20480
	ds_read_b128 v[12:15], v66 offset:26624
	global_load_lds_dwordx4 v59, s[30:31]
	s_add_u32 s30, s30, 0x80
	s_addc_u32 s31, s31, 0
	ds_read_b128 v[16:19], v63 offset:24576
	ds_read_b128 v[20:23], v67 offset:24576
	ds_read_b128 v[24:27], v67 offset:26624
	s_waitcnt lgkmcnt(3)
	v_mfma_f32_16x16x32_f16 v[28:31], v[4:7], v[8:11], v[28:31]
	v_mfma_f32_16x16x32_f16 v[32:35], v[4:7], v[12:15], v[32:35]
	s_waitcnt lgkmcnt(0)
	v_mfma_f32_16x16x32_f16 v[28:31], v[16:19], v[20:23], v[28:31]
	v_mfma_f32_16x16x32_f16 v[32:35], v[16:19], v[24:27], v[32:35]
	s_waitcnt vmcnt(18)
	s_barrier
	s_add_i32 m0, s18, 24576
	ds_read_b128 v[4:7], v62 offset:36864
	global_load_lds_dwordx4 v[130:131], off
	s_add_i32 m0, s18, 28672
	ds_read_b128 v[8:11], v66 offset:36864
	global_load_lds_dwordx4 v58, s[30:31]
	s_add_i32 m0, s18, 32768
	ds_read_b128 v[12:15], v66 offset:38912
	global_load_lds_dwordx4 v59, s[30:31]
	s_add_u32 s30, s30, 0x80
	s_addc_u32 s31, s31, 0
	ds_read_b128 v[16:19], v63 offset:36864
	ds_read_b128 v[20:23], v67 offset:36864
	ds_read_b128 v[24:27], v67 offset:38912
	s_waitcnt lgkmcnt(3)
	v_mfma_f32_16x16x32_f16 v[28:31], v[4:7], v[8:11], v[28:31]
	v_mfma_f32_16x16x32_f16 v[32:35], v[4:7], v[12:15], v[32:35]
	s_waitcnt lgkmcnt(0)
	v_mfma_f32_16x16x32_f16 v[28:31], v[16:19], v[20:23], v[28:31]
	v_mfma_f32_16x16x32_f16 v[32:35], v[16:19], v[24:27], v[32:35]
	s_waitcnt vmcnt(18)
	s_barrier
	s_add_i32 m0, s18, 36864
	ds_read_b128 v[4:7], v64
	global_load_lds_dwordx4 v[132:133], off
	s_add_i32 m0, s18, 40960
	ds_read_b128 v[8:11], v68
	global_load_lds_dwordx4 v58, s[30:31]
	s_add_i32 m0, s18, 45056
	ds_read_b128 v[12:15], v68 offset:2048
	global_load_lds_dwordx4 v59, s[30:31]
	s_add_u32 s30, s30, 0x80
	s_addc_u32 s31, s31, 0
	ds_read_b128 v[16:19], v65
	ds_read_b128 v[20:23], v69
	ds_read_b128 v[24:27], v69 offset:2048
	s_waitcnt lgkmcnt(3)
	v_mfma_f32_16x16x32_f16 v[28:31], v[4:7], v[8:11], v[28:31]
	v_mfma_f32_16x16x32_f16 v[32:35], v[4:7], v[12:15], v[32:35]
	s_waitcnt lgkmcnt(0)
	v_mfma_f32_16x16x32_f16 v[28:31], v[16:19], v[20:23], v[28:31]
	v_mfma_f32_16x16x32_f16 v[32:35], v[16:19], v[24:27], v[32:35]
	s_waitcnt vmcnt(18)
	s_barrier
	s_add_i32 m0, s18, 49152
	ds_read_b128 v[4:7], v64 offset:12288
	global_load_lds_dwordx4 v[134:135], off
	s_add_i32 m0, s18, 53248
	ds_read_b128 v[8:11], v68 offset:12288
	global_load_lds_dwordx4 v58, s[30:31]
	s_add_i32 m0, s18, 57344
	ds_read_b128 v[12:15], v68 offset:14336
	global_load_lds_dwordx4 v59, s[30:31]
	s_add_u32 s30, s30, 0x80
	s_addc_u32 s31, s31, 0
	ds_read_b128 v[16:19], v65 offset:12288
	ds_read_b128 v[20:23], v69 offset:12288
	ds_read_b128 v[24:27], v69 offset:14336
	s_waitcnt lgkmcnt(3)
	v_mfma_f32_16x16x32_f16 v[28:31], v[4:7], v[8:11], v[28:31]
	v_mfma_f32_16x16x32_f16 v[32:35], v[4:7], v[12:15], v[32:35]
	s_waitcnt lgkmcnt(0)
	v_mfma_f32_16x16x32_f16 v[28:31], v[16:19], v[20:23], v[28:31]
	v_mfma_f32_16x16x32_f16 v[32:35], v[16:19], v[24:27], v[32:35]
	s_waitcnt vmcnt(18)
	s_barrier
	s_add_i32 m0, s18, 61440
	ds_read_b128 v[4:7], v64 offset:24576
	global_load_lds_dwordx4 v[136:137], off
	s_add_i32 m0, s18, 65536
	ds_read_b128 v[8:11], v68 offset:24576
	global_load_lds_dwordx4 v58, s[30:31]
	s_add_i32 m0, s18, 69632
	ds_read_b128 v[12:15], v68 offset:26624
	global_load_lds_dwordx4 v59, s[30:31]
	s_add_u32 s30, s30, 0x80
	s_addc_u32 s31, s31, 0
	ds_read_b128 v[16:19], v65 offset:24576
	ds_read_b128 v[20:23], v69 offset:24576
	ds_read_b128 v[24:27], v69 offset:26624
	s_waitcnt lgkmcnt(3)
	v_mfma_f32_16x16x32_f16 v[28:31], v[4:7], v[8:11], v[28:31]
	v_mfma_f32_16x16x32_f16 v[32:35], v[4:7], v[12:15], v[32:35]
	s_waitcnt lgkmcnt(0)
	v_mfma_f32_16x16x32_f16 v[28:31], v[16:19], v[20:23], v[28:31]
	v_mfma_f32_16x16x32_f16 v[32:35], v[16:19], v[24:27], v[32:35]
	s_waitcnt vmcnt(18)
	s_barrier
	s_add_i32 m0, s18, 73728
	ds_read_b128 v[4:7], v64 offset:36864
	global_load_lds_dwordx4 v[138:139], off
	s_add_i32 m0, s18, 77824
	ds_read_b128 v[8:11], v68 offset:36864
	global_load_lds_dwordx4 v58, s[30:31]
	s_add_i32 m0, s18, 81920
	ds_read_b128 v[12:15], v68 offset:38912
	global_load_lds_dwordx4 v59, s[30:31]
	s_add_u32 s30, s30, 0x80
	s_addc_u32 s31, s31, 0
	ds_read_b128 v[16:19], v65 offset:36864
	ds_read_b128 v[20:23], v69 offset:36864
	ds_read_b128 v[24:27], v69 offset:38912
	s_waitcnt lgkmcnt(3)
	v_mfma_f32_16x16x32_f16 v[28:31], v[4:7], v[8:11], v[28:31]
	v_mfma_f32_16x16x32_f16 v[32:35], v[4:7], v[12:15], v[32:35]
	s_waitcnt lgkmcnt(0)
	v_mfma_f32_16x16x32_f16 v[28:31], v[16:19], v[20:23], v[28:31]
	v_mfma_f32_16x16x32_f16 v[32:35], v[16:19], v[24:27], v[32:35]
	s_waitcnt vmcnt(18)
	s_barrier
	s_add_i32 m0, s18, 86016
	ds_read_b128 v[4:7], v62
	global_load_lds_dwordx4 v[140:141], off
	s_add_i32 m0, s18, 90112
	ds_read_b128 v[8:11], v66
	global_load_lds_dwordx4 v58, s[30:31]
	s_add_i32 m0, s18, 94208
	ds_read_b128 v[12:15], v66 offset:2048
	global_load_lds_dwordx4 v59, s[30:31]
	s_add_u32 s30, s30, 0x80
	s_addc_u32 s31, s31, 0
	ds_read_b128 v[16:19], v63
	ds_read_b128 v[20:23], v67
	ds_read_b128 v[24:27], v67 offset:2048
	s_waitcnt lgkmcnt(3)
	v_mfma_f32_16x16x32_f16 v[28:31], v[4:7], v[8:11], v[28:31]
	v_mfma_f32_16x16x32_f16 v[32:35], v[4:7], v[12:15], v[32:35]
	s_waitcnt lgkmcnt(0)
	v_mfma_f32_16x16x32_f16 v[28:31], v[16:19], v[20:23], v[28:31]
	v_mfma_f32_16x16x32_f16 v[32:35], v[16:19], v[24:27], v[32:35]
	s_waitcnt vmcnt(18)
	s_barrier
	s_mov_b32 m0, s18
	ds_read_b128 v[4:7], v62 offset:12288
	global_load_lds_dwordx4 v[142:143], off
	s_add_i32 m0, s18, 4096
	ds_read_b128 v[8:11], v66 offset:12288
	global_load_lds_dwordx4 v58, s[30:31]
	s_add_i32 m0, s18, 8192
	ds_read_b128 v[12:15], v66 offset:14336
	global_load_lds_dwordx4 v59, s[30:31]
	s_add_u32 s30, s30, 0x80
	s_addc_u32 s31, s31, 0
	ds_read_b128 v[16:19], v63 offset:12288
	ds_read_b128 v[20:23], v67 offset:12288
	ds_read_b128 v[24:27], v67 offset:14336
	s_waitcnt lgkmcnt(3)
	v_mfma_f32_16x16x32_f16 v[28:31], v[4:7], v[8:11], v[28:31]
	v_mfma_f32_16x16x32_f16 v[32:35], v[4:7], v[12:15], v[32:35]
	s_waitcnt lgkmcnt(0)
	v_mfma_f32_16x16x32_f16 v[28:31], v[16:19], v[20:23], v[28:31]
	v_mfma_f32_16x16x32_f16 v[32:35], v[16:19], v[24:27], v[32:35]
	s_waitcnt vmcnt(18)
	s_barrier
	s_add_i32 m0, s18, 12288
	ds_read_b128 v[4:7], v62 offset:24576
	global_load_lds_dwordx4 v[144:145], off
	s_add_i32 m0, s18, 16384
	ds_read_b128 v[8:11], v66 offset:24576
	global_load_lds_dwordx4 v58, s[30:31]
	s_add_i32 m0, s18, 20480
	ds_read_b128 v[12:15], v66 offset:26624
	global_load_lds_dwordx4 v59, s[30:31]
	s_add_u32 s30, s30, 0x80
	s_addc_u32 s31, s31, 0
	ds_read_b128 v[16:19], v63 offset:24576
	ds_read_b128 v[20:23], v67 offset:24576
	ds_read_b128 v[24:27], v67 offset:26624
	s_waitcnt lgkmcnt(3)
	v_mfma_f32_16x16x32_f16 v[28:31], v[4:7], v[8:11], v[28:31]
	v_mfma_f32_16x16x32_f16 v[32:35], v[4:7], v[12:15], v[32:35]
	s_waitcnt lgkmcnt(0)
	v_mfma_f32_16x16x32_f16 v[28:31], v[16:19], v[20:23], v[28:31]
	v_mfma_f32_16x16x32_f16 v[32:35], v[16:19], v[24:27], v[32:35]
	s_waitcnt vmcnt(18)
	s_barrier
	ds_read_b128 v[4:7], v62 offset:36864
	ds_read_b128 v[8:11], v66 offset:36864
	ds_read_b128 v[12:15], v66 offset:38912
	ds_read_b128 v[16:19], v63 offset:36864
	ds_read_b128 v[20:23], v67 offset:36864
	ds_read_b128 v[24:27], v67 offset:38912
	s_waitcnt lgkmcnt(3)
	v_mfma_f32_16x16x32_f16 v[28:31], v[4:7], v[8:11], v[28:31]
	v_mfma_f32_16x16x32_f16 v[32:35], v[4:7], v[12:15], v[32:35]
	s_waitcnt lgkmcnt(0)
	v_mfma_f32_16x16x32_f16 v[28:31], v[16:19], v[20:23], v[28:31]
	v_mfma_f32_16x16x32_f16 v[32:35], v[16:19], v[24:27], v[32:35]
	s_waitcnt vmcnt(15)
	s_barrier
	ds_read_b128 v[4:7], v64
	ds_read_b128 v[8:11], v68
	ds_read_b128 v[12:15], v68 offset:2048
	ds_read_b128 v[16:19], v65
	ds_read_b128 v[20:23], v69
	ds_read_b128 v[24:27], v69 offset:2048
	s_waitcnt lgkmcnt(3)
	v_mfma_f32_16x16x32_f16 v[28:31], v[4:7], v[8:11], v[28:31]
	v_mfma_f32_16x16x32_f16 v[32:35], v[4:7], v[12:15], v[32:35]
	s_waitcnt lgkmcnt(0)
	v_mfma_f32_16x16x32_f16 v[28:31], v[16:19], v[20:23], v[28:31]
	v_mfma_f32_16x16x32_f16 v[32:35], v[16:19], v[24:27], v[32:35]
	s_waitcnt vmcnt(12)
	s_barrier
	ds_read_b128 v[4:7], v64 offset:12288
	ds_read_b128 v[8:11], v68 offset:12288
	ds_read_b128 v[12:15], v68 offset:14336
	ds_read_b128 v[16:19], v65 offset:12288
	ds_read_b128 v[20:23], v69 offset:12288
	ds_read_b128 v[24:27], v69 offset:14336
	s_waitcnt lgkmcnt(3)
	v_mfma_f32_16x16x32_f16 v[28:31], v[4:7], v[8:11], v[28:31]
	v_mfma_f32_16x16x32_f16 v[32:35], v[4:7], v[12:15], v[32:35]
	s_waitcnt lgkmcnt(0)
	v_mfma_f32_16x16x32_f16 v[28:31], v[16:19], v[20:23], v[28:31]
	v_mfma_f32_16x16x32_f16 v[32:35], v[16:19], v[24:27], v[32:35]
	s_waitcnt vmcnt(9)
	s_barrier
	ds_read_b128 v[4:7], v64 offset:24576
	ds_read_b128 v[8:11], v68 offset:24576
	ds_read_b128 v[12:15], v68 offset:26624
	ds_read_b128 v[16:19], v65 offset:24576
	ds_read_b128 v[20:23], v69 offset:24576
	ds_read_b128 v[24:27], v69 offset:26624
	s_waitcnt lgkmcnt(3)
	v_mfma_f32_16x16x32_f16 v[28:31], v[4:7], v[8:11], v[28:31]
	v_mfma_f32_16x16x32_f16 v[32:35], v[4:7], v[12:15], v[32:35]
	s_waitcnt lgkmcnt(0)
	v_mfma_f32_16x16x32_f16 v[28:31], v[16:19], v[20:23], v[28:31]
	v_mfma_f32_16x16x32_f16 v[32:35], v[16:19], v[24:27], v[32:35]
	s_waitcnt vmcnt(6)
	s_barrier
	ds_read_b128 v[4:7], v64 offset:36864
	ds_read_b128 v[8:11], v68 offset:36864
	ds_read_b128 v[12:15], v68 offset:38912
	ds_read_b128 v[16:19], v65 offset:36864
	ds_read_b128 v[20:23], v69 offset:36864
	ds_read_b128 v[24:27], v69 offset:38912
	s_waitcnt lgkmcnt(3)
	v_mfma_f32_16x16x32_f16 v[28:31], v[4:7], v[8:11], v[28:31]
	v_mfma_f32_16x16x32_f16 v[32:35], v[4:7], v[12:15], v[32:35]
	s_waitcnt lgkmcnt(0)
	v_mfma_f32_16x16x32_f16 v[28:31], v[16:19], v[20:23], v[28:31]
	v_mfma_f32_16x16x32_f16 v[32:35], v[16:19], v[24:27], v[32:35]
	s_waitcnt vmcnt(3)
	s_barrier
	ds_read_b128 v[4:7], v62
	ds_read_b128 v[8:11], v66
	ds_read_b128 v[12:15], v66 offset:2048
	ds_read_b128 v[16:19], v63
	ds_read_b128 v[20:23], v67
	ds_read_b128 v[24:27], v67 offset:2048
	s_waitcnt lgkmcnt(3)
	v_mfma_f32_16x16x32_f16 v[28:31], v[4:7], v[8:11], v[28:31]
	v_mfma_f32_16x16x32_f16 v[32:35], v[4:7], v[12:15], v[32:35]
	s_waitcnt lgkmcnt(0)
	v_mfma_f32_16x16x32_f16 v[28:31], v[16:19], v[20:23], v[28:31]
	v_mfma_f32_16x16x32_f16 v[32:35], v[16:19], v[24:27], v[32:35]
	s_waitcnt vmcnt(0)
	s_barrier
	ds_read_b128 v[4:7], v62 offset:12288
	ds_read_b128 v[8:11], v66 offset:12288
	ds_read_b128 v[12:15], v66 offset:14336
	ds_read_b128 v[16:19], v63 offset:12288
	ds_read_b128 v[20:23], v67 offset:12288
	ds_read_b128 v[24:27], v67 offset:14336
	s_waitcnt lgkmcnt(3)
	v_mfma_f32_16x16x32_f16 v[28:31], v[4:7], v[8:11], v[28:31]
	v_mfma_f32_16x16x32_f16 v[32:35], v[4:7], v[12:15], v[32:35]
	s_waitcnt lgkmcnt(0)
	v_mfma_f32_16x16x32_f16 v[28:31], v[16:19], v[20:23], v[28:31]
	v_mfma_f32_16x16x32_f16 v[32:35], v[16:19], v[24:27], v[32:35]
	s_lshl_b32 s24, s22, 0
	v_lshl_add_u32 v103, v2, 2, s22
	s_movk_i32 s25, 0x90
	v_mul_lo_u32 v103, v103, s25
	v_add_u32_e32 v104, s23, v1
	v_lshl_add_u32 v103, v104, 1, v103
	v_lshrrev_b32_e32 v105, 3, v0
	v_mul_lo_u32 v105, v105, s25
	v_and_b32_e32 v106, 7, v0
	v_lshl_add_u32 v105, v106, 4, v105
	s_waitcnt vmcnt(0) lgkmcnt(0)
	s_barrier
	s_nop 7
	s_nop 7
	v_add_f32_e32 v28, v36, v28
	v_max_f32_e32 v28, 0, v28
	v_cvt_f16_f32_e32 v28, v28
	v_add_f32_e32 v29, v36, v29
	v_max_f32_e32 v29, 0, v29
	v_cvt_f16_f32_e32 v29, v29
	v_add_f32_e32 v30, v36, v30
	v_max_f32_e32 v30, 0, v30
	v_cvt_f16_f32_e32 v30, v30
	v_add_f32_e32 v31, v36, v31
	v_max_f32_e32 v31, 0, v31
	v_cvt_f16_f32_e32 v31, v31
	v_add_f32_e32 v32, v37, v32
	v_max_f32_e32 v32, 0, v32
	v_cvt_f16_f32_e32 v32, v32
	v_add_f32_e32 v33, v37, v33
	v_max_f32_e32 v33, 0, v33
	v_cvt_f16_f32_e32 v33, v33
	v_add_f32_e32 v34, v37, v34
	v_max_f32_e32 v34, 0, v34
	v_cvt_f16_f32_e32 v34, v34
	v_add_f32_e32 v35, v37, v35
	v_max_f32_e32 v35, 0, v35
	v_cvt_f16_f32_e32 v35, v35
	ds_write_b16 v103, v28
	ds_write_b16 v103, v29 offset:144
	ds_write_b16 v103, v30 offset:288
	ds_write_b16 v103, v31 offset:432
	ds_write_b16 v103, v32 offset:32
	ds_write_b16 v103, v33 offset:176
	ds_write_b16 v103, v34 offset:320
	ds_write_b16 v103, v35 offset:464
	s_waitcnt lgkmcnt(0)
	s_barrier
	ds_read_b128 v[4:7], v105
	s_waitcnt lgkmcnt(0)
	v_pk_add_f16 v4, v4, v70
	v_pk_add_f16 v5, v5, v71
	v_pk_add_f16 v6, v6, v72
	v_pk_add_f16 v7, v7, v73
	global_store_dwordx4 v[96:97], v[4:7], off
	s_endpgm

	.amdhsa_kernel _Z6gemm_gILi32ELi64ELi16ELi32ELi1ELi1ELi64ELi4EEv5GemmP
		.amdhsa_group_segment_fixed_size 98304
		.amdhsa_private_segment_fixed_size 0
		.amdhsa_kernarg_size 112
		.amdhsa_user_sgpr_count 2
		.amdhsa_user_sgpr_dispatch_ptr 0
		.amdhsa_user_sgpr_queue_ptr 0
		.amdhsa_user_sgpr_kernarg_segment_ptr 1
		.amdhsa_user_sgpr_dispatch_id 0
		.amdhsa_user_sgpr_kernarg_preload_length 0
		.amdhsa_user_sgpr_kernarg_preload_offset 0
		.amdhsa_user_sgpr_private_segment_size 0
		.amdhsa_uses_dynamic_stack 0
		.amdhsa_enable_private_segment 0
		.amdhsa_system_sgpr_workgroup_id_x 1
		.amdhsa_system_sgpr_workgroup_id_y 1
		.amdhsa_system_sgpr_workgroup_id_z 0
		.amdhsa_system_sgpr_workgroup_info 0
		.amdhsa_system_vgpr_workitem_id 0
		.amdhsa_next_free_vgpr 148
		.amdhsa_next_free_sgpr 96
		.amdhsa_accum_offset 148
		.amdhsa_reserve_vcc 1
		.amdhsa_float_round_mode_32 0
		.amdhsa_float_round_mode_16_64 0
		.amdhsa_float_denorm_mode_32 3
		.amdhsa_float_denorm_mode_16_64 3
		.amdhsa_dx10_clamp 1
		.amdhsa_ieee_mode 1
		.amdhsa_fp16_overflow 0
		.amdhsa_tg_split 0
		.amdhsa_exception_fp_ieee_invalid_op 0
		.amdhsa_exception_fp_denorm_src 0
		.amdhsa_exception_fp_ieee_div_zero 0
		.amdhsa_exception_fp_ieee_overflow 0
		.amdhsa_exception_fp_ieee_underflow 0
		.amdhsa_exception_fp_ieee_inexact 0
		.amdhsa_exception_int_div_zero 0
	.end_amdhsa_kernel

amdhsa.kernels:
  - .agpr_count:     0
    .args:
      - .offset:         0
        .size:           152
        .value_kind:     by_value
    .group_segment_fixed_size: 7168
    .kernarg_segment_align: 8
    .kernarg_segment_size: 152
    .language:       OpenCL C
    .language_version:
      - 2
      - 0
    .max_flat_workgroup_size: 256
    .name:           _Z6prep_k5PrepP
    .private_segment_fixed_size: 0
    .sgpr_count:     62
    .sgpr_spill_count: 0
    .symbol:         _Z6prep_k5PrepP.kd
    .uniform_work_group_size: 1
    .uses_dynamic_stack: false
    .vgpr_count:     58
    .vgpr_spill_count: 0
    .wavefront_size: 64
  - .agpr_count:     0
    .args:
      - .actual_access:  read_only
        .address_space:  global
        .offset:         0
        .size:           8
        .value_kind:     global_buffer
      - .actual_access:  read_only
        .address_space:  global
        .offset:         8
        .size:           8
        .value_kind:     global_buffer
      - .actual_access:  read_only
        .address_space:  global
        .offset:         16
        .size:           8
        .value_kind:     global_buffer
      - .actual_access:  write_only
        .address_space:  global
        .offset:         24
        .size:           8
        .value_kind:     global_buffer
      - .actual_access:  write_only
        .address_space:  global
        .offset:         32
        .size:           8
        .value_kind:     global_buffer
    .group_segment_fixed_size: 9216
    .kernarg_segment_align: 8
    .kernarg_segment_size: 40
    .language:       OpenCL C
    .language_version:
      - 2
      - 0
    .max_flat_workgroup_size: 256
    .name:           _Z8conv1d_kPKDF16_PKfS2_PDF16_S3_
    .private_segment_fixed_size: 0
    .sgpr_count:     22
    .sgpr_spill_count: 0
    .symbol:         _Z8conv1d_kPKDF16_PKfS2_PDF16_S3_.kd
    .uniform_work_group_size: 1
    .uses_dynamic_stack: false
    .vgpr_count:     53
    .vgpr_spill_count: 0
    .wavefront_size: 64
  - .agpr_count:     0
    .args:
      - .actual_access:  read_only
        .address_space:  global
        .offset:         0
        .size:           8
        .value_kind:     global_buffer
      - .actual_access:  read_only
        .address_space:  global
        .offset:         8
        .size:           8
        .value_kind:     global_buffer
      - .actual_access:  read_only
        .address_space:  global
        .offset:         16
        .size:           8
        .value_kind:     global_buffer
      - .actual_access:  read_only
        .address_space:  global
        .offset:         24
        .size:           8
        .value_kind:     global_buffer
      - .actual_access:  write_only
        .address_space:  global
        .offset:         32
        .size:           8
        .value_kind:     global_buffer
      - .actual_access:  write_only
        .address_space:  global
        .offset:         40
        .size:           8
        .value_kind:     global_buffer
    .group_segment_fixed_size: 70656
    .kernarg_segment_align: 8
    .kernarg_segment_size: 48
    .language:       OpenCL C
    .language_version:
      - 2
      - 0
    .max_flat_workgroup_size: 256
    .name:           _Z4dt_kPKfS0_S0_PKDF16_PDF16_S3_
    .private_segment_fixed_size: 0
    .sgpr_count:     25
    .sgpr_spill_count: 0
    .symbol:         _Z4dt_kPKfS0_S0_PKDF16_PDF16_S3_.kd
    .uniform_work_group_size: 1
    .uses_dynamic_stack: false
    .vgpr_count:     96
    .vgpr_spill_count: 0
    .wavefront_size: 64
  - .agpr_count:     0
    .args:
      - .address_space:  global
        .offset:         0
        .size:           8
        .value_kind:     global_buffer
      - .actual_access:  read_only
        .address_space:  global
        .offset:         8
        .size:           8
        .value_kind:     global_buffer
      - .address_space:  global
        .offset:         16
        .size:           8
        .value_kind:     global_buffer
      - .address_space:  global
        .offset:         24
        .size:           8
        .value_kind:     global_buffer
      - .actual_access:  read_only
        .address_space:  global
        .offset:         32
        .size:           8
        .value_kind:     global_buffer
      - .actual_access:  write_only
        .address_space:  global
        .offset:         40
        .size:           8
        .value_kind:     global_buffer
    .group_segment_fixed_size: 86016
    .kernarg_segment_align: 8
    .kernarg_segment_size: 48
    .language:       OpenCL C
    .language_version:
      - 2
      - 0
    .max_flat_workgroup_size: 256
    .name:           _Z6scan_kPKDF16_S0_S0_S0_PKfPf
    .private_segment_fixed_size: 0
    .sgpr_count:     66
    .sgpr_spill_count: 0
    .symbol:         _Z6scan_kPKDF16_S0_S0_S0_PKfPf.kd
    .uniform_work_group_size: 1
    .uses_dynamic_stack: false
    .vgpr_count:     200
    .vgpr_spill_count: 0
    .wavefront_size: 64
  - .agpr_count:     0
    .args:
      - .actual_access:  read_only
        .address_space:  global
        .offset:         0
        .size:           8
        .value_kind:     global_buffer
      - .actual_access:  read_only
        .address_space:  global
        .offset:         8
        .size:           8
        .value_kind:     global_buffer
      - .actual_access:  read_only
        .address_space:  global
        .offset:         16
        .size:           8
        .value_kind:     global_buffer
      - .actual_access:  read_only
        .address_space:  global
        .offset:         24
        .size:           8
        .value_kind:     global_buffer
      - .actual_access:  write_only
        .address_space:  global
        .offset:         32
        .size:           8
        .value_kind:     global_buffer
    .group_segment_fixed_size: 9216
    .kernarg_segment_align: 8
    .kernarg_segment_size: 40
    .language:       OpenCL C
    .language_version:
      - 2
      - 0
    .max_flat_workgroup_size: 256
    .name:           _Z6gate_kPKfPKDF16_S2_S0_PDF16_
    .private_segment_fixed_size: 0
    .sgpr_count:     22
    .sgpr_spill_count: 0
    .symbol:         _Z6gate_kPKfPKDF16_S2_S0_PDF16_.kd
    .uniform_work_group_size: 1
    .uses_dynamic_stack: false
    .vgpr_count:     46
    .vgpr_spill_count: 0
    .wavefront_size: 64
  - .agpr_count:     0
    .args:
      - .actual_access:  read_only
        .address_space:  global
        .offset:         0
        .size:           8
        .value_kind:     global_buffer
      - .actual_access:  read_only
        .address_space:  global
        .offset:         8
        .size:           8
        .value_kind:     global_buffer
      - .actual_access:  read_only
        .address_space:  global
        .offset:         16
        .size:           8
        .value_kind:     global_buffer
      - .actual_access:  write_only
        .address_space:  global
        .offset:         24
        .size:           8
        .value_kind:     global_buffer
    .group_segment_fixed_size: 6912
    .kernarg_segment_align: 8
    .kernarg_segment_size: 32
    .language:       OpenCL C
    .language_version:
      - 2
      - 0
    .max_flat_workgroup_size: 256
    .name:           _Z9deconv3_kPKDF16_PKfS2_Pf
    .private_segment_fixed_size: 0
    .sgpr_count:     26
    .sgpr_spill_count: 0
    .symbol:         _Z9deconv3_kPKDF16_PKfS2_Pf.kd
    .uniform_work_group_size: 1
    .uses_dynamic_stack: false
    .vgpr_count:     55
    .vgpr_spill_count: 0
    .wavefront_size: 64
  - .agpr_count:     8
    .args:
      - .offset:         0
        .size:           112
        .value_kind:     by_value
    .group_segment_fixed_size: 49152
    .kernarg_segment_align: 8
    .kernarg_segment_size: 112
    .language:       OpenCL C
    .language_version:
      - 2
      - 0
    .max_flat_workgroup_size: 256
    .name:           _Z6gemm_gILi32ELi64ELi16ELi32ELi1ELi0ELi64ELi4EEv5GemmP
    .private_segment_fixed_size: 0
    .sgpr_count:     34
    .sgpr_spill_count: 0
    .symbol:         _Z6gemm_gILi32ELi64ELi16ELi32ELi1ELi0ELi64ELi4EEv5GemmP.kd
    .uniform_work_group_size: 1
    .uses_dynamic_stack: false
    .vgpr_count:     40
    .vgpr_spill_count: 0
    .wavefront_size: 64
  - .agpr_count:     16
    .args:
      - .offset:         0
        .size:           112
        .value_kind:     by_value
    .group_segment_fixed_size: 65536
    .kernarg_segment_align: 8
    .kernarg_segment_size: 112
    .language:       OpenCL C
    .language_version:
      - 2
      - 0
    .max_flat_workgroup_size: 256
    .name:           _Z6gemm_gILi64ELi64ELi32ELi32ELi1ELi0ELi64ELi4EEv5GemmP
    .private_segment_fixed_size: 0
    .sgpr_count:     34
    .sgpr_spill_count: 0
    .symbol:         _Z6gemm_gILi64ELi64ELi32ELi32ELi1ELi0ELi64ELi4EEv5GemmP.kd
    .uniform_work_group_size: 1
    .uses_dynamic_stack: false
    .vgpr_count:     56
    .vgpr_spill_count: 0
    .wavefront_size: 64
  - .agpr_count:     32
    .args:
      - .offset:         0
        .size:           112
        .value_kind:     by_value
    .group_segment_fixed_size: 73728
    .kernarg_segment_align: 8
    .kernarg_segment_size: 112
    .language:       OpenCL C
    .language_version:
      - 2
      - 0
    .max_flat_workgroup_size: 256
    .name:           _Z6gemm_gILi64ELi128ELi32ELi64ELi0ELi2ELi64ELi3EEv5GemmP
    .private_segment_fixed_size: 0
    .sgpr_count:     27
    .sgpr_spill_count: 0
    .symbol:         _Z6gemm_gILi64ELi128ELi32ELi64ELi0ELi2ELi64ELi3EEv5GemmP.kd
    .uniform_work_group_size: 1
    .uses_dynamic_stack: false
    .vgpr_count:     80
    .vgpr_spill_count: 0
    .wavefront_size: 64
  - .agpr_count:     16
    .args:
      - .offset:         0
        .size:           112
        .value_kind:     by_value
    .group_segment_fixed_size: 49152
    .kernarg_segment_align: 8
    .kernarg_segment_size: 112
    .language:       OpenCL C
    .language_version:
      - 2
      - 0
    .max_flat_workgroup_size: 256
    .name:           _Z6gemm_gILi64ELi64ELi32ELi32ELi0ELi3ELi64ELi3EEv5GemmP
    .private_segment_fixed_size: 0
    .sgpr_count:     30
    .sgpr_spill_count: 0
    .symbol:         _Z6gemm_gILi64ELi64ELi32ELi32ELi0ELi3ELi64ELi3EEv5GemmP.kd
    .uniform_work_group_size: 1
    .uses_dynamic_stack: false
    .vgpr_count:     56
    .vgpr_spill_count: 0
    .wavefront_size: 64
  - .agpr_count:     16
    .args:
      - .offset:         0
        .size:           112
        .value_kind:     by_value
    .group_segment_fixed_size: 49152
    .kernarg_segment_align: 8
    .kernarg_segment_size: 112
    .language:       OpenCL C
    .language_version:
      - 2
      - 0
    .max_flat_workgroup_size: 256
    .name:           _Z6gemm_gILi64ELi64ELi32ELi32ELi0ELi4ELi64ELi3EEv5GemmP
    .private_segment_fixed_size: 0
    .sgpr_count:     27
    .sgpr_spill_count: 0
    .symbol:         _Z6gemm_gILi64ELi64ELi32ELi32ELi0ELi4ELi64ELi3EEv5GemmP.kd
    .uniform_work_group_size: 1
    .uses_dynamic_stack: false
    .vgpr_count:     52
    .vgpr_spill_count: 0
    .wavefront_size: 64
  - .agpr_count:     8
    .args:
      - .offset:         0
        .size:           112
        .value_kind:     by_value
    .group_segment_fixed_size: 73728
    .kernarg_segment_align: 8
    .kernarg_segment_size: 112
    .language:       OpenCL C
    .language_version:
      - 2
      - 0
    .max_flat_workgroup_size: 256
    .name:           _Z6gemm_gILi32ELi64ELi16ELi32ELi1ELi1ELi128ELi3EEv5GemmP
    .private_segment_fixed_size: 0
    .sgpr_count:     38
    .sgpr_spill_count: 0
    .symbol:         _Z6gemm_gILi32ELi64ELi16ELi32ELi1ELi1ELi128ELi3EEv5GemmP.kd
    .uniform_work_group_size: 1
    .uses_dynamic_stack: false
    .vgpr_count:     48
    .vgpr_spill_count: 0
    .wavefront_size: 64
  - .agpr_count:     0
    .args:
      - .offset:         0
        .size:           112
        .value_kind:     by_value
    .group_segment_fixed_size: 98304
    .kernarg_segment_align: 8
    .kernarg_segment_size: 112
    .language:       OpenCL C
    .language_version:
      - 2
      - 0
    .max_flat_workgroup_size: 256
    .name:           _Z6gemm_gILi32ELi64ELi16ELi32ELi1ELi1ELi64ELi4EEv5GemmP
    .private_segment_fixed_size: 0
    .sgpr_count:     36
    .sgpr_spill_count: 0
    .symbol:         _Z6gemm_gILi32ELi64ELi16ELi32ELi1ELi1ELi64ELi4EEv5GemmP.kd
    .uniform_work_group_size: 1
    .uses_dynamic_stack: false
    .vgpr_count:     148
    .vgpr_spill_count: 0
    .wavefront_size: 64
